# diff/swa unit loops: v_pk_add/mul/fma_f32 replaced by scalar f32 pairs (bit-identical)
# baseline (speedup 1.0000x reference)
; #define LAS __attribute__((address_space(3)))
; __device__ __forceinline__ float bflo(unsigned w) { return __uint_as_float(w << 16); }
; __device__ __forceinline__ float bfhi(unsigned w) { return __uint_as_float(w & 0xFFFF0000u); }
; __device__ __forceinline__ unsigned pkbf(float lo, float hi) { f32x2_t v = {lo, hi}; bf16x2_t b = __builtin_convertvector(v, bf16x2_t); return __builtin_bit_cast(unsigned, b); }
;     ...
;         const int u = *ucur;
;         if (u >= 17 * 32) break;
;         const int qi = 16 - u / 32, bh = u % 32, b = bh >> 2, h = bh & 3;
;         const int q0 = qi == 0 ? 0 : 16 + 256 * (qi - 1), nkt = qi == 0 ? 1 : 4 * qi + 1;
;         const int q0w = q0 + 32 * wave, qpos = q0w + l31;
;         const bool wave_on = (qi > 0) || (wave == 0);
;         const size_t qrow = (size_t)b * LT + (qpos < LT ? qpos : LT - 1);
;         LAS bf16x8* Qs = (LAS bf16x8*)(lds + 4096 + 4 * DF_KB) + wave * 384 + lane;
;         const float farb = btab[h * 132 + 128] * c2;
;         float mref[2];
;         { const unsigned* kmx = (const unsigned*)(ws + WS_CTL) + CW_KMX + l * 256 + b * 8 + h * 2;
; #pragma unroll
;           for (int c = 0; c < 2; ++c) { float qn2 = 0.f;
; #pragma unroll
;               for (int s = 0; s < 2; ++s) { const u32x4 qv = *(const u32x4*)(U + qrow * INW + C_QD + h * 64 + c * 32 + s * 16 + hi * 8);
;                   const unsigned qw[4] = {qv.x, qv.y, qv.z, qv.w};
;                   { u32x4 qs; qs.x = pkbf(bflo(qw[0]) * c2, bfhi(qw[0]) * c2); qs.y = pkbf(bflo(qw[1]) * c2, bfhi(qw[1]) * c2); qs.z = pkbf(bflo(qw[2]) * c2, bfhi(qw[2]) * c2); qs.w = pkbf(bflo(qw[3]) * c2, bfhi(qw[3]) * c2);
;                     Qs[(c * 2 + s) * 64] = __builtin_bit_cast(bf16x8, qs); }
; #pragma unroll
;                   for (int e = 0; e < 4; ++e) qn2 += bflo(qw[e]) * bflo(qw[e]) + bfhi(qw[e]) * bfhi(qw[e]); }
;               qn2 += __shfl_xor(qn2, 32);
;               const float km2 = __uint_as_float(__hip_atomic_load(kmx + c, __ATOMIC_RELAXED, __HIP_MEMORY_SCOPE_AGENT));
;               mref[c] = (sqrtf(qn2 * km2) * 1.001f + btab[h * 132 + 129]) * c2;
;               { u32x4 qx; qx.x = hi ? 0u : (pkbf(farb - mref[c], 0.f) & 0xffffu); qx.y = 0u; qx.z = 0u; qx.w = 0u; Qs[(4 + c) * 64] = __builtin_bit_cast(bf16x8, qx); } } }
.LBB0_774:
	s_or_b64 exec, exec, s[0:1]
	s_waitcnt lgkmcnt(0)
	s_barrier
	ds_read_b32 v0, v1 offset:2112
	s_movk_i32 s0, 0x21f
	s_waitcnt lgkmcnt(0)
	v_cmp_lt_i32_e32 vcc, s0, v0
	v_readfirstlane_b32 s30, v0
	s_mov_b64 s[0:1], -1
	s_cbranch_vccnz .LBB0_769
	s_ashr_i32 s0, s30, 31
	s_lshr_b32 s0, s0, 27
	s_add_i32 s0, s30, s0
	s_ashr_i32 s35, s0, 5
	s_andn2_b32 s0, s0, 31
	s_sub_i32 s34, s30, s0
	s_lshl_b32 s1, s35, 8
	s_sub_i32 s31, 16, s35
	s_ashr_i32 s0, s34, 2
	s_and_b32 s36, s34, 3
	s_sub_i32 s1, 0xf10, s1
	s_cmp_lg_u32 s31, 0
	s_cselect_b32 s49, s1, 0
	s_add_i32 s49, s49, s46
	s_mul_i32 s22, s0, 0x1010
	s_mul_i32 s1, s36, 0x210
	s_lshl_b32 s0, s0, 3
	v_add_u32_e32 v148, s49, v149
	s_add_i32 s50, s1, 0
	s_ashr_i32 s1, s0, 31
	s_ashr_i32 s23, s22, 31
	v_min_i32_e32 v2, 0x100f, v148
	s_lshl_b64 s[0:1], s[0:1], 2
	v_ashrrev_i32_e32 v3, 31, v2
	s_add_u32 s0, s47, s0
	v_lshl_add_u64 v[2:3], v[2:3], 0, s[22:23]
	s_addc_u32 s1, s48, s1
	s_lshl_b32 s28, s36, 3
	v_mov_b64_e32 v[4:5], s[8:9]
	s_add_u32 s24, s0, s28
	v_mad_u64_u32 v[4:5], s[38:39], v2, s97, v[4:5]
	s_addc_u32 s25, s1, 0
	v_mad_i32_i24 v5, v3, s97, v5
	s_lshl_b32 s40, s36, 7
	v_lshl_add_u64 v[2:3], v[4:5], 0, s[40:41]
	v_mov_b32_e32 v147, v1
	v_lshl_add_u64 v[4:5], v[2:3], 0, v[146:147]
	global_load_dwordx4 v[6:9], v[4:5], off offset:1024
	global_load_dwordx4 v[112:115], v[4:5], off offset:1056
	v_mov_b32_e32 v125, s28
	s_mul_i32 s58, s22, 0x1600
	global_load_dword v124, v125, s[0:1] sc1
	s_mul_hi_i32 s59, s22, 0x1600
	global_load_dwordx4 v[116:119], v[4:5], off offset:1088
	s_add_u32 s58, s8, s58
	s_addc_u32 s59, s9, s59
	global_load_dwordx4 v[120:123], v[4:5], off offset:1120
	s_lshl_b32 s60, s36, 7
	s_add_u32 s58, s58, s60
	s_addc_u32 s59, s59, 0
	global_load_dword v126, v1, s[24:25] offset:4 sc1
	s_mul_i32 s60, s34, 0x41000
	s_ashr_i32 s61, s60, 31
	s_lshl_b64 s[60:61], s[60:61], 1
	s_add_u32 s60, s42, s60
	s_addc_u32 s61, s43, s61
	v_lshl_add_u64 v[66:67], v[142:143], 1, s[58:59]
	v_lshl_add_u64 v[68:69], v[144:145], 1, s[60:61]
	global_load_dwordx4 v[102:105], v[66:67], off offset:1536
	global_load_dwordx4 v[106:109], v[68:69], off
	v_mov_b32_e32 v0, s50
	ds_read_b32 v0, v0 offset:512
	v_and_b32_e32 v2, 64, v222
	v_add_u32_e32 v2, 64, v2
	s_waitcnt lgkmcnt(0)
	v_mul_f32_e32 v12, 0x3e8293ee, v0
	v_xor_b32_e32 v0, 32, v222
	v_cmp_lt_i32_e32 vcc, v0, v2
	s_waitcnt vmcnt(7)
	v_lshlrev_b32_e32 v2, 16, v6
	v_and_b32_e32 v3, 0xffff0000, v6
	v_mul_f32_e32 v10, s92, v2
	v_mul_f32_e32 v11, s92, v3
	v_mul_f32_e32 v2, v2, v2
	v_mul_f32_e32 v3, v3, v3
	v_cvt_pk_bf16_f32 v6, v10, v11
	v_lshlrev_b32_e32 v10, 16, v7
	v_and_b32_e32 v11, 0xffff0000, v7
	v_mul_f32_e32 v14, s92, v10
	v_mul_f32_e32 v15, s92, v11
	v_add_f32_e32 v2, v2, v3
	v_cvt_pk_bf16_f32 v7, v14, v15
	v_lshlrev_b32_e32 v14, 16, v8
	v_and_b32_e32 v15, 0xffff0000, v8
	v_mul_f32_e32 v16, s92, v14
	v_mul_f32_e32 v17, s92, v15
	v_cndmask_b32_e32 v0, v222, v0, vcc
	v_cvt_pk_bf16_f32 v8, v16, v17
	v_lshlrev_b32_e32 v16, 16, v9
	v_and_b32_e32 v17, 0xffff0000, v9
	v_mul_f32_e32 v18, s92, v16
	v_mul_f32_e32 v19, s92, v17
	v_lshlrev_b32_e32 v190, 2, v0
	v_cvt_pk_bf16_f32 v9, v18, v19
	ds_write_b128 v189, v[6:9] offset:40960
	v_mul_f32_e32 v8, v10, v10
	v_mul_f32_e32 v9, v11, v11
	v_mul_f32_e32 v6, v14, v14
	v_mul_f32_e32 v7, v15, v15
	v_mul_f32_e32 v10, v16, v16
	v_mul_f32_e32 v11, v17, v17
	v_add_f32_e32 v8, v8, v9
	v_add_f32_e32 v2, v2, v8
	v_add_f32_e32 v3, v6, v7
	v_add_f32_e32 v0, v10, v11
	v_add_f32_e32 v2, v3, v2
	v_add_f32_e32 v0, v0, v2
	s_waitcnt vmcnt(6)
	v_mov_b64_e32 v[14:15], v[112:113]
	v_mov_b64_e32 v[16:17], v[114:115]
	v_lshlrev_b32_e32 v18, 16, v14
	v_and_b32_e32 v19, 0xffff0000, v14
	v_mul_f32_e32 v20, s92, v18
	v_mul_f32_e32 v21, s92, v19
	s_nop 0
	v_cvt_pk_bf16_f32 v14, v20, v21
	v_lshlrev_b32_e32 v20, 16, v15
	v_and_b32_e32 v21, 0xffff0000, v15
	v_mul_f32_e32 v22, s92, v20
	v_mul_f32_e32 v23, s92, v21
	s_nop 0
	v_cvt_pk_bf16_f32 v15, v22, v23
	v_lshlrev_b32_e32 v22, 16, v16
	v_and_b32_e32 v23, 0xffff0000, v16
	v_mul_f32_e32 v24, s92, v22
	v_mul_f32_e32 v25, s92, v23
	s_nop 0
	v_cvt_pk_bf16_f32 v16, v24, v25
	v_lshlrev_b32_e32 v24, 16, v17
	v_and_b32_e32 v25, 0xffff0000, v17
	v_mul_f32_e32 v26, s92, v24
	v_mul_f32_e32 v27, s92, v25
	s_nop 0
	v_cvt_pk_bf16_f32 v17, v26, v27
	ds_write_b128 v189, v[14:17] offset:41984
	v_mul_f32_e32 v14, v18, v18
	v_mul_f32_e32 v15, v19, v19
	v_mul_f32_e32 v16, v20, v20
	v_mul_f32_e32 v17, v21, v21
	v_add_f32_e32 v2, v14, v15
	v_mul_f32_e32 v18, v22, v22
	v_mul_f32_e32 v19, v23, v23
	v_add_f32_e32 v0, v2, v0
	v_add_f32_e32 v2, v16, v17
	v_mul_f32_e32 v20, v24, v24
	v_mul_f32_e32 v21, v25, v25
	v_add_f32_e32 v0, v2, v0
	v_add_f32_e32 v2, v18, v19
	v_add_f32_e32 v0, v2, v0
	v_add_f32_e32 v2, v20, v21
	v_add_f32_e32 v2, v2, v0
	v_mov_b32_e32 v0, s28
	ds_bpermute_b32 v3, v190, v2
	v_mov_b32_e32 v18, 0
	v_mov_b32_e32 v0, 0
	s_and_saveexec_b64 s[28:29], s[4:5]
	s_cbranch_execz .LBB0_777
	s_waitcnt lgkmcnt(0)
	v_add_f32_e32 v0, v2, v3
	s_waitcnt vmcnt(5)
	v_mul_f32_e32 v0, v0, v124
	s_mov_b32 s0, 0xf800000
	v_mul_f32_e32 v2, 0x4f800000, v0
	v_cmp_gt_f32_e32 vcc, s0, v0
	s_nop 1
	v_cndmask_b32_e32 v0, v0, v2, vcc
	v_sqrt_f32_e32 v2, v0
	s_nop 0
	v_add_u32_e32 v3, -1, v2
	v_fma_f32 v7, -v3, v2, v0
	v_add_u32_e32 v6, 1, v2
	v_cmp_ge_f32_e64 s[0:1], 0, v7
	s_nop 1
	v_cndmask_b32_e64 v3, v2, v3, s[0:1]
	v_fma_f32 v2, -v6, v2, v0
	v_cmp_lt_f32_e64 s[0:1], 0, v2
	s_nop 1
	v_cndmask_b32_e64 v2, v3, v6, s[0:1]
	v_mov_b32_e32 v3, s50
	ds_read_b32 v3, v3 offset:516
	v_mul_f32_e32 v6, 0x37800000, v2
	v_cndmask_b32_e32 v2, v2, v6, vcc
	v_cmp_class_f32_e32 vcc, v0, v250
	s_nop 1
	v_cndmask_b32_e32 v0, v2, v0, vcc
	s_waitcnt lgkmcnt(0)
	v_fmac_f32_e32 v3, 0x3f8020c5, v0
	v_fmamk_f32 v0, v3, 0xbe8293ee, v12
	v_cvt_pk_bf16_f32 v0, v0, 0
	v_and_b32_e32 v0, 0xffff, v0
; __device__ __forceinline__ float bflo(unsigned w) { return __uint_as_float(w << 16); }
; __device__ __forceinline__ float bfhi(unsigned w) { return __uint_as_float(w & 0xFFFF0000u); }
; __device__ __forceinline__ unsigned pkbf(float lo, float hi) { f32x2_t v = {lo, hi}; bf16x2_t b = __builtin_convertvector(v, bf16x2_t); return __builtin_bit_cast(unsigned, b); }
;     ...
;           for (int c = 0; c < 2; ++c) { float qn2 = 0.f;
; #pragma unroll
;               for (int s = 0; s < 2; ++s) { const u32x4 qv = *(const u32x4*)(U + qrow * INW + C_QD + h * 64 + c * 32 + s * 16 + hi * 8);
;                   const unsigned qw[4] = {qv.x, qv.y, qv.z, qv.w};
;                   { u32x4 qs; qs.x = pkbf(bflo(qw[0]) * c2, bfhi(qw[0]) * c2); qs.y = pkbf(bflo(qw[1]) * c2, bfhi(qw[1]) * c2); qs.z = pkbf(bflo(qw[2]) * c2, bfhi(qw[2]) * c2); qs.w = pkbf(bflo(qw[3]) * c2, bfhi(qw[3]) * c2);
;                     Qs[(c * 2 + s) * 64] = __builtin_bit_cast(bf16x8, qs); }
; #pragma unroll
;                   for (int e = 0; e < 4; ++e) qn2 += bflo(qw[e]) * bflo(qw[e]) + bfhi(qw[e]) * bfhi(qw[e]); }
;               qn2 += __shfl_xor(qn2, 32);
;               const float km2 = __uint_as_float(__hip_atomic_load(kmx + c, __ATOMIC_RELAXED, __HIP_MEMORY_SCOPE_AGENT));
;               mref[c] = (sqrtf(qn2 * km2) * 1.001f + btab[h * 132 + 129]) * c2;
;               { u32x4 qx; qx.x = hi ? 0u : (pkbf(farb - mref[c], 0.f) & 0xffffu); qx.y = 0u; qx.z = 0u; qx.w = 0u; Qs[(4 + c) * 64] = __builtin_bit_cast(bf16x8, qx); } } }
.LBB0_777:
	s_or_b64 exec, exec, s[28:29]
	v_mov_b32_e32 v2, v1
	s_waitcnt lgkmcnt(0)
	v_mov_b32_e32 v3, v1
	ds_write_b128 v189, v[0:3] offset:45056
	s_mov_b32 s51, 0
	s_waitcnt vmcnt(4)
	v_mov_b64_e32 v[6:7], v[116:117]
	v_mov_b64_e32 v[8:9], v[118:119]
	v_lshlrev_b32_e32 v2, 16, v6
	v_and_b32_e32 v3, 0xffff0000, v6
	v_mul_f32_e32 v10, s92, v2
	v_mul_f32_e32 v11, s92, v3
	v_mul_f32_e32 v2, v2, v2
	v_mul_f32_e32 v3, v3, v3
	v_cvt_pk_bf16_f32 v6, v10, v11
	v_lshlrev_b32_e32 v10, 16, v7
	v_and_b32_e32 v11, 0xffff0000, v7
	v_mul_f32_e32 v14, s92, v10
	v_mul_f32_e32 v15, s92, v11
	v_add_f32_e32 v2, v2, v3
	v_cvt_pk_bf16_f32 v7, v14, v15
	v_lshlrev_b32_e32 v14, 16, v8
	v_and_b32_e32 v15, 0xffff0000, v8
	v_mul_f32_e32 v16, s92, v14
	v_mul_f32_e32 v17, s92, v15
	s_nop 0
	v_cvt_pk_bf16_f32 v8, v16, v17
	v_lshlrev_b32_e32 v16, 16, v9
	v_and_b32_e32 v17, 0xffff0000, v9
	v_mul_f32_e32 v20, s92, v16
	v_mul_f32_e32 v21, s92, v17
	s_nop 0
	v_cvt_pk_bf16_f32 v9, v20, v21
	ds_write_b128 v189, v[6:9] offset:43008
	v_mul_f32_e32 v8, v10, v10
	v_mul_f32_e32 v9, v11, v11
	v_mul_f32_e32 v6, v14, v14
	v_mul_f32_e32 v7, v15, v15
	v_mul_f32_e32 v10, v16, v16
	v_mul_f32_e32 v11, v17, v17
	v_add_f32_e32 v8, v8, v9
	v_add_f32_e32 v2, v2, v8
	v_add_f32_e32 v3, v6, v7
	v_add_f32_e32 v2, v3, v2
	v_add_f32_e32 v0, v10, v11
	v_add_f32_e32 v0, v0, v2
	s_waitcnt vmcnt(3)
	v_mov_b64_e32 v[14:15], v[120:121]
	v_mov_b64_e32 v[16:17], v[122:123]
	v_lshlrev_b32_e32 v4, 16, v14
	v_and_b32_e32 v5, 0xffff0000, v14
	v_mul_f32_e32 v20, s92, v4
	v_mul_f32_e32 v21, s92, v5
	v_mul_f32_e32 v4, v4, v4
	v_mul_f32_e32 v5, v5, v5
	v_cvt_pk_bf16_f32 v14, v20, v21
	v_lshlrev_b32_e32 v20, 16, v15
	v_and_b32_e32 v21, 0xffff0000, v15
	v_mul_f32_e32 v22, s92, v20
	v_mul_f32_e32 v23, s92, v21
	v_add_f32_e32 v2, v4, v5
	v_cvt_pk_bf16_f32 v15, v22, v23
	v_lshlrev_b32_e32 v22, 16, v16
	v_and_b32_e32 v23, 0xffff0000, v16
	v_mul_f32_e32 v24, s92, v22
	v_mul_f32_e32 v25, s92, v23
	v_add_f32_e32 v0, v2, v0
	v_cvt_pk_bf16_f32 v16, v24, v25
	v_lshlrev_b32_e32 v24, 16, v17
	v_and_b32_e32 v25, 0xffff0000, v17
	v_mul_f32_e32 v26, s92, v24
	v_mul_f32_e32 v27, s92, v25
	s_nop 0
	v_cvt_pk_bf16_f32 v17, v26, v27
	ds_write_b128 v189, v[14:17] offset:44032
	v_mul_f32_e32 v14, v20, v20
	v_mul_f32_e32 v15, v21, v21
	v_mul_f32_e32 v16, v22, v22
	v_mul_f32_e32 v17, v23, v23
	v_add_f32_e32 v2, v14, v15
	v_mul_f32_e32 v20, v24, v24
	v_mul_f32_e32 v21, v25, v25
	v_add_f32_e32 v0, v2, v0
	v_add_f32_e32 v2, v16, v17
	v_add_f32_e32 v0, v2, v0
	v_add_f32_e32 v2, v20, v21
	v_add_f32_e32 v0, v2, v0
	ds_bpermute_b32 v2, v190, v0
	s_and_saveexec_b64 s[24:25], s[4:5]
	s_cbranch_execz .LBB0_779
	s_waitcnt lgkmcnt(0)
	v_add_f32_e32 v0, v0, v2
	s_waitcnt vmcnt(2)
	v_mul_f32_e32 v0, v0, v126
	s_mov_b32 s0, 0xf800000
	v_mul_f32_e32 v2, 0x4f800000, v0
	v_cmp_gt_f32_e32 vcc, s0, v0
	s_nop 1
	v_cndmask_b32_e32 v0, v0, v2, vcc
	v_sqrt_f32_e32 v2, v0
	s_nop 0
	v_add_u32_e32 v3, -1, v2
	v_fma_f32 v5, -v3, v2, v0
	v_add_u32_e32 v4, 1, v2
	v_cmp_ge_f32_e64 s[0:1], 0, v5
	s_nop 1
	v_cndmask_b32_e64 v3, v2, v3, s[0:1]
	v_fma_f32 v2, -v4, v2, v0
	v_cmp_lt_f32_e64 s[0:1], 0, v2
	s_nop 1
	v_cndmask_b32_e64 v2, v3, v4, s[0:1]
	v_mov_b32_e32 v3, s50
	ds_read_b32 v3, v3 offset:516
	v_mul_f32_e32 v4, 0x37800000, v2
	v_cndmask_b32_e32 v2, v2, v4, vcc
	v_cmp_class_f32_e32 vcc, v0, v250
	s_nop 1
	v_cndmask_b32_e32 v0, v2, v0, vcc
	s_waitcnt lgkmcnt(0)
	v_fmac_f32_e32 v3, 0x3f8020c5, v0
	v_fmac_f32_e32 v12, 0xbe8293ee, v3
	v_cvt_pk_bf16_f32 v0, v12, 0
	v_and_b32_e32 v18, 0xffff, v0

; #define LAS __attribute__((address_space(3)))
; __device__ __forceinline__ void diff_tile(const bool near, const LAS unsigned char* Kb, const LAS unsigned char* Vb, const LAS float* btab, const LAS bf16x8* Qs, f32x16 (&O)[2][2],
;                                           float (&lsum)[2], int qpos, int k0, int l31, int hi, float c2, float farraw) {
;     float bm[2][16];
;     if (near) {
; #pragma unroll
;         for (int kb = 0; kb < 2; ++kb)
; #pragma unroll
;             for (int r = 0; r < 16; ++r) { const int dist = qpos - (k0 + 32 * kb + (r & 3) + 8 * (r >> 2) + 4 * hi); bm[kb][r] = btab[min(max(dist, 0), 128)]; }
; #pragma unroll
;         for (int kb = 0; kb < 2; ++kb)
; #pragma unroll
;             for (int r = 0; r < 16; ++r) { asm volatile("" : "+v"(bm[kb][r]));
;                 const int dist = qpos - (k0 + 32 * kb + (r & 3) + 8 * (r >> 2) + 4 * hi); bm[kb][r] = dist < 0 ? -INFINITY : (bm[kb][r] - farraw) * c2; }
;     ...
;         for (int kt = 0; kt < nkt; ++kt) {
;             const int k0 = kt * 64, cur = kt & 1;
;             if (kt + 1 < nkt) { kreg = *(const u32x4*)(kbase + (koff + (unsigned)((k0 + 64) * INW))); vreg = *(const u32x4*)(vbase + (voff + (unsigned)(k0 + 64))); }
;             if (wave_on && k0 <= q0w + 31) {
;                 const LAS unsigned char* Kb = KV + cur * DF_KB; const LAS unsigned char* Vb = KV + (2 + cur) * DF_KB;
;                 diff_tile(q0w - (k0 + 63) < 113, Kb, Vb, btab + h * 132, Qs, O, lsum, qpos, k0, l31, hi, c2, farraw);
.LBB0_783:
	s_and_b32 s57, s56, 1
	s_cmp_le_i32 s51, s53
	s_cselect_b64 s[0:1], -1, 0
	s_and_b64 s[0:1], s[28:29], s[0:1]
	s_andn2_b64 vcc, exec, s[0:1]
	s_cbranch_vccnz .LBB0_791
	s_cmpk_lt_i32 s54, 0x71
	s_cselect_b64 s[38:39], -1, 0
	s_cmpk_gt_i32 s54, 0x70
	s_cbranch_scc1 .LBB0_786
	v_add_u32_e32 v96, s51, v186
	v_sub_u32_e32 v66, v149, v186
	v_add_u32_e32 v66, s54, v66
	v_or_b32_e32 v97, 3, v96
	v_or_b32_e32 v110, 2, v96
	v_or_b32_e32 v111, 9, v96
	v_or_b32_e32 v112, 8, v96
	v_or_b32_e32 v113, 11, v96
	v_or_b32_e32 v114, 10, v96
	v_or_b32_e32 v115, 17, v96
	v_or_b32_e32 v116, 16, v96
	v_or_b32_e32 v117, 19, v96
	v_or_b32_e32 v118, 18, v96
	v_or_b32_e32 v119, 25, v96
	v_or_b32_e32 v120, 24, v96
	v_or_b32_e32 v121, 27, v96
	v_or_b32_e32 v122, 26, v96
	v_or_b32_e32 v123, 33, v96
	v_or_b32_e32 v124, 32, v96
	v_or_b32_e32 v125, 35, v96
	v_or_b32_e32 v126, 34, v96
	v_or_b32_e32 v127, 41, v96
	v_or_b32_e32 v128, 40, v96
	v_or_b32_e32 v129, 43, v96
	v_or_b32_e32 v130, 42, v96
	v_or_b32_e32 v131, 49, v96
	v_or_b32_e32 v132, 48, v96
	v_or_b32_e32 v133, 51, v96
	v_or_b32_e32 v134, 50, v96
	v_or_b32_e32 v135, 57, v96
	v_or_b32_e32 v136, 56, v96
	v_add_u32_e32 v67, 63, v66
	v_add_u32_e32 v66, 62, v66
	v_sub_u32_e32 v68, v148, v110
	v_sub_u32_e32 v69, v148, v97
	v_sub_u32_e32 v70, v148, v112
	v_sub_u32_e32 v71, v148, v111
	v_sub_u32_e32 v72, v148, v114
	v_sub_u32_e32 v73, v148, v113
	v_sub_u32_e32 v74, v148, v116
	v_sub_u32_e32 v75, v148, v115
	v_sub_u32_e32 v76, v148, v118
	v_sub_u32_e32 v77, v148, v117
	v_sub_u32_e32 v78, v148, v120
	v_sub_u32_e32 v79, v148, v119
	v_sub_u32_e32 v80, v148, v122
	v_sub_u32_e32 v81, v148, v121
	v_sub_u32_e32 v82, v148, v124
	v_sub_u32_e32 v83, v148, v123
	v_sub_u32_e32 v84, v148, v126
	v_sub_u32_e32 v85, v148, v125
	v_sub_u32_e32 v86, v148, v128
	v_sub_u32_e32 v87, v148, v127
	v_sub_u32_e32 v88, v148, v130
	v_sub_u32_e32 v89, v148, v129
	v_sub_u32_e32 v90, v148, v132
	v_sub_u32_e32 v91, v148, v131
	v_sub_u32_e32 v92, v148, v134
	v_sub_u32_e32 v93, v148, v133
	v_sub_u32_e32 v94, v148, v136
	v_sub_u32_e32 v95, v148, v135
	v_or_b32_e32 v137, 59, v96
	v_or_b32_e32 v138, 58, v96
	v_med3_i32 v67, v67, 0, v218
	v_med3_i32 v66, v66, 0, v218
	v_med3_i32 v68, v68, 0, v218
	v_med3_i32 v69, v69, 0, v218
	v_med3_i32 v70, v70, 0, v218
	v_med3_i32 v71, v71, 0, v218
	v_med3_i32 v72, v72, 0, v218
	v_med3_i32 v73, v73, 0, v218
	v_med3_i32 v74, v74, 0, v218
	v_med3_i32 v75, v75, 0, v218
	v_med3_i32 v76, v76, 0, v218
	v_med3_i32 v77, v77, 0, v218
	v_med3_i32 v78, v78, 0, v218
	v_med3_i32 v79, v79, 0, v218
	v_med3_i32 v80, v80, 0, v218
	v_med3_i32 v81, v81, 0, v218
	v_med3_i32 v82, v82, 0, v218
	v_med3_i32 v83, v83, 0, v218
	v_med3_i32 v84, v84, 0, v218
	v_med3_i32 v85, v85, 0, v218
	v_med3_i32 v86, v86, 0, v218
	v_med3_i32 v87, v87, 0, v218
	v_med3_i32 v88, v88, 0, v218
	v_med3_i32 v89, v89, 0, v218
	v_med3_i32 v90, v90, 0, v218
	v_med3_i32 v91, v91, 0, v218
	v_med3_i32 v92, v92, 0, v218
	v_med3_i32 v93, v93, 0, v218
	v_med3_i32 v94, v94, 0, v218
	v_med3_i32 v95, v95, 0, v218
	v_sub_u32_e32 v139, v148, v138
	v_sub_u32_e32 v140, v148, v137
	v_lshl_add_u32 v67, v67, 2, s50
	v_lshl_add_u32 v66, v66, 2, s50
	v_lshl_add_u32 v68, v68, 2, s50
	v_lshl_add_u32 v69, v69, 2, s50
	v_lshl_add_u32 v70, v70, 2, s50
	v_lshl_add_u32 v71, v71, 2, s50
	v_lshl_add_u32 v72, v72, 2, s50
	v_lshl_add_u32 v73, v73, 2, s50
	v_lshl_add_u32 v74, v74, 2, s50
	v_lshl_add_u32 v75, v75, 2, s50
	v_lshl_add_u32 v76, v76, 2, s50
	v_lshl_add_u32 v77, v77, 2, s50
	v_lshl_add_u32 v78, v78, 2, s50
	v_lshl_add_u32 v79, v79, 2, s50
	v_lshl_add_u32 v80, v80, 2, s50
	v_lshl_add_u32 v81, v81, 2, s50
	v_lshl_add_u32 v82, v82, 2, s50
	v_lshl_add_u32 v83, v83, 2, s50
	v_lshl_add_u32 v84, v84, 2, s50
	v_lshl_add_u32 v85, v85, 2, s50
	v_lshl_add_u32 v86, v86, 2, s50
	v_lshl_add_u32 v87, v87, 2, s50
	v_lshl_add_u32 v88, v88, 2, s50
	v_lshl_add_u32 v89, v89, 2, s50
	v_lshl_add_u32 v90, v90, 2, s50
	v_lshl_add_u32 v91, v91, 2, s50
	v_lshl_add_u32 v92, v92, 2, s50
	v_lshl_add_u32 v93, v93, 2, s50
	v_lshl_add_u32 v94, v94, 2, s50
	v_lshl_add_u32 v95, v95, 2, s50
	v_med3_i32 v139, v139, 0, v218
	v_med3_i32 v140, v140, 0, v218
	v_lshl_add_u32 v139, v139, 2, s50
	v_lshl_add_u32 v140, v140, 2, s50
	ds_read_b32 v141, v67
	ds_read_b32 v152, v66
	ds_read_b32 v66, v68
	ds_read_b32 v67, v69
	ds_read_b32 v68, v70
	ds_read_b32 v69, v71
	ds_read_b32 v70, v72
	ds_read_b32 v71, v73
	ds_read_b32 v72, v74
	ds_read_b32 v73, v75
	ds_read_b32 v74, v76
	ds_read_b32 v75, v77
	ds_read_b32 v76, v78
	ds_read_b32 v77, v79
	ds_read_b32 v78, v80
	ds_read_b32 v79, v81
	ds_read_b32 v80, v82
	ds_read_b32 v81, v83
	ds_read_b32 v82, v84
	ds_read_b32 v83, v85
	ds_read_b32 v84, v86
	ds_read_b32 v85, v87
	ds_read_b32 v86, v88
	ds_read_b32 v87, v89
	ds_read_b32 v88, v90
	ds_read_b32 v89, v91
	ds_read_b32 v90, v92
	ds_read_b32 v91, v93
	ds_read_b32 v92, v94
	ds_read_b32 v93, v95
	ds_read_b32 v94, v139
	ds_read_b32 v95, v140
	s_waitcnt lgkmcnt(14)
	v_cmp_ge_i32_e32 vcc, v148, v96
	v_sub_f32_e32 v139, v141, v150
	v_mul_f32_e32 v139, 0x3e8293ee, v139
	v_sub_f32_e32 v140, v152, v150
	v_mul_f32_e32 v140, 0x3e8293ee, v140
	v_cndmask_b32_e32 v152, v219, v139, vcc
	v_cmp_lt_i32_e32 vcc, v96, v148
	v_sub_f32_e32 v66, v66, v150
	v_sub_f32_e32 v67, v67, v151
	s_nop 0
	v_cndmask_b32_e32 v153, v219, v140, vcc
	v_mul_f32_e32 v66, s92, v66
	v_mul_f32_e32 v67, s92, v67
	v_cmp_ge_i32_e32 vcc, v148, v110
	s_nop 1
	v_cndmask_b32_e32 v154, v219, v66, vcc
	v_cmp_ge_i32_e32 vcc, v147, v97
	s_nop 1
	v_cndmask_b32_e32 v155, v219, v67, vcc
	v_sub_f32_e32 v66, v68, v150
	v_sub_f32_e32 v67, v69, v151
	v_cmp_ge_i32_e32 vcc, v148, v112
	v_mul_f32_e32 v66, s92, v66
	v_mul_f32_e32 v67, s92, v67
	s_waitcnt lgkmcnt(13)
; __device__ __forceinline__ void diff_tile(const bool near, const LAS unsigned char* Kb, const LAS unsigned char* Vb, const LAS float* btab, const LAS bf16x8* Qs, f32x16 (&O)[2][2],
;                                           float (&lsum)[2], int qpos, int k0, int l31, int hi, float c2, float farraw) {
;     ...
;             for (int r = 0; r < 16; ++r) { const int dist = qpos - (k0 + 32 * kb + (r & 3) + 8 * (r >> 2) + 4 * hi); bm[kb][r] = btab[min(max(dist, 0), 128)]; }
; #pragma unroll
;         for (int kb = 0; kb < 2; ++kb)
; #pragma unroll
;             for (int r = 0; r < 16; ++r) { asm volatile("" : "+v"(bm[kb][r]));
;                 const int dist = qpos - (k0 + 32 * kb + (r & 3) + 8 * (r >> 2) + 4 * hi); bm[kb][r] = dist < 0 ? -INFINITY : (bm[kb][r] - farraw) * c2; }
	s_waitcnt lgkmcnt(12)
	s_waitcnt lgkmcnt(11)
	s_waitcnt lgkmcnt(10)
	s_waitcnt lgkmcnt(9)
	v_cndmask_b32_e32 v156, v219, v66, vcc
	v_cmp_ge_i32_e32 vcc, v147, v111
	s_waitcnt lgkmcnt(8)
	s_waitcnt lgkmcnt(7)
	s_waitcnt lgkmcnt(6)
	s_waitcnt lgkmcnt(5)
	s_waitcnt lgkmcnt(4)
	v_cndmask_b32_e32 v157, v219, v67, vcc
	v_sub_f32_e32 v66, v70, v150
	v_sub_f32_e32 v67, v71, v151
	v_cmp_ge_i32_e32 vcc, v148, v114
	v_mul_f32_e32 v66, s92, v66
	v_mul_f32_e32 v67, s92, v67
	s_waitcnt lgkmcnt(3)
	s_waitcnt lgkmcnt(2)
	s_waitcnt lgkmcnt(1)
	s_waitcnt lgkmcnt(0)
	v_cndmask_b32_e32 v158, v219, v66, vcc
	v_cmp_ge_i32_e32 vcc, v147, v113
	s_nop 1
	v_cndmask_b32_e32 v159, v219, v67, vcc
	v_sub_f32_e32 v66, v72, v150
	v_sub_f32_e32 v67, v73, v151
	v_cmp_ge_i32_e32 vcc, v148, v116
	v_mul_f32_e32 v66, s92, v66
	v_mul_f32_e32 v67, s92, v67
	s_nop 0
	v_cndmask_b32_e32 v160, v219, v66, vcc
	v_cmp_ge_i32_e32 vcc, v147, v115
	s_nop 1
	v_cndmask_b32_e32 v161, v219, v67, vcc
	v_sub_f32_e32 v66, v74, v150
	v_sub_f32_e32 v67, v75, v151
	v_cmp_ge_i32_e32 vcc, v148, v118
	v_mul_f32_e32 v66, s92, v66
	v_mul_f32_e32 v67, s92, v67
	s_nop 0
	v_cndmask_b32_e32 v162, v219, v66, vcc
	v_cmp_ge_i32_e32 vcc, v147, v117
	s_nop 1
	v_cndmask_b32_e32 v163, v219, v67, vcc
	v_sub_f32_e32 v66, v76, v150
	v_sub_f32_e32 v67, v77, v151
	v_cmp_ge_i32_e32 vcc, v148, v120
	v_mul_f32_e32 v66, s92, v66
	v_mul_f32_e32 v67, s92, v67
	s_nop 0
	v_cndmask_b32_e32 v164, v219, v66, vcc
	v_cmp_ge_i32_e32 vcc, v147, v119
	s_nop 1
	v_cndmask_b32_e32 v165, v219, v67, vcc
	v_sub_f32_e32 v66, v78, v150
	v_sub_f32_e32 v67, v79, v151
	v_cmp_ge_i32_e32 vcc, v148, v122
	v_mul_f32_e32 v66, s92, v66
	v_mul_f32_e32 v67, s92, v67
	s_nop 0
	v_cndmask_b32_e32 v166, v219, v66, vcc
	v_cmp_ge_i32_e32 vcc, v147, v121
	s_nop 1
	v_cndmask_b32_e32 v167, v219, v67, vcc
	v_sub_f32_e32 v66, v80, v150
	v_sub_f32_e32 v67, v81, v151
	v_cmp_ge_i32_e32 vcc, v148, v124
	v_mul_f32_e32 v66, s92, v66
	v_mul_f32_e32 v67, s92, v67
	s_nop 0
	v_cndmask_b32_e32 v168, v219, v66, vcc
	v_cmp_ge_i32_e32 vcc, v147, v123
	s_nop 1
	v_cndmask_b32_e32 v169, v219, v67, vcc
	v_sub_f32_e32 v66, v82, v150
	v_sub_f32_e32 v67, v83, v151
	v_cmp_ge_i32_e32 vcc, v148, v126
	v_mul_f32_e32 v66, s92, v66
	v_mul_f32_e32 v67, s92, v67
	s_nop 0
	v_cndmask_b32_e32 v170, v219, v66, vcc
	v_cmp_ge_i32_e32 vcc, v147, v125
	s_nop 1
	v_cndmask_b32_e32 v171, v219, v67, vcc
	v_sub_f32_e32 v66, v84, v150
	v_sub_f32_e32 v67, v85, v151
	v_cmp_ge_i32_e32 vcc, v148, v128
	v_mul_f32_e32 v66, s92, v66
	v_mul_f32_e32 v67, s92, v67
	s_nop 0
	v_cndmask_b32_e32 v172, v219, v66, vcc
	v_cmp_ge_i32_e32 vcc, v147, v127
	s_nop 1
	v_cndmask_b32_e32 v173, v219, v67, vcc
	v_sub_f32_e32 v66, v86, v150
	v_sub_f32_e32 v67, v87, v151
	v_cmp_ge_i32_e32 vcc, v148, v130
	v_mul_f32_e32 v66, s92, v66
	v_mul_f32_e32 v67, s92, v67
	s_nop 0
	v_cndmask_b32_e32 v174, v219, v66, vcc
	v_cmp_ge_i32_e32 vcc, v147, v129
	s_nop 1
	v_cndmask_b32_e32 v175, v219, v67, vcc
	v_sub_f32_e32 v66, v88, v150
	v_sub_f32_e32 v67, v89, v151
	v_cmp_ge_i32_e32 vcc, v148, v132
	v_mul_f32_e32 v66, s92, v66
	v_mul_f32_e32 v67, s92, v67
	s_nop 0
	v_cndmask_b32_e32 v176, v219, v66, vcc
	v_cmp_ge_i32_e32 vcc, v147, v131
	s_nop 1
	v_cndmask_b32_e32 v177, v219, v67, vcc
	v_sub_f32_e32 v66, v90, v150
	v_sub_f32_e32 v67, v91, v151
	v_cmp_ge_i32_e32 vcc, v148, v134
	v_mul_f32_e32 v66, s92, v66
	v_mul_f32_e32 v67, s92, v67
	s_nop 0
	v_cndmask_b32_e32 v178, v219, v66, vcc
	v_cmp_ge_i32_e32 vcc, v147, v133
	s_nop 1
	v_cndmask_b32_e32 v179, v219, v67, vcc
	v_sub_f32_e32 v66, v92, v150
	v_sub_f32_e32 v67, v93, v151
	v_cmp_ge_i32_e32 vcc, v148, v136
	v_mul_f32_e32 v66, s92, v66
	v_mul_f32_e32 v67, s92, v67
	s_nop 0
	v_cndmask_b32_e32 v180, v219, v66, vcc
	v_cmp_ge_i32_e32 vcc, v147, v135
	s_nop 1
	v_cndmask_b32_e32 v181, v219, v67, vcc
	v_sub_f32_e32 v66, v94, v150
	v_sub_f32_e32 v67, v95, v151
	v_cmp_ge_i32_e32 vcc, v148, v138
	v_mul_f32_e32 v66, s92, v66
	v_mul_f32_e32 v67, s92, v67
	s_nop 0
	v_cndmask_b32_e32 v182, v219, v66, vcc
	v_cmp_ge_i32_e32 vcc, v147, v137
	s_nop 1
	v_cndmask_b32_e32 v183, v219, v67, vcc
; #define LAS __attribute__((address_space(3)))
; __device__ __forceinline__ void diff_tile(const bool near, const LAS unsigned char* Kb, const LAS unsigned char* Vb, const LAS float* btab, const LAS bf16x8* Qs, f32x16 (&O)[2][2],
;                                           float (&lsum)[2], int qpos, int k0, int l31, int hi, float c2, float farraw) {
;     ...
;     for (int c = 0; c < 2; ++c) {
;         f32x16 S[2];
; #pragma unroll
;         for (int kb = 0; kb < 2; ++kb) {
;             f32x16 acc;
; #pragma unroll
;             for (int r = 0; r < 16; ++r) acc[r] = 0.f;
; #pragma unroll
;             for (int s = 0; s < 2; ++s) { const bf16x8 kf = *(const LAS bf16x8*)(Kb + (32 * kb + l31) * DF_PITCH + c * 64 + s * 32 + hi * 16);
;                 acc = __builtin_amdgcn_mfma_f32_32x32x16_bf16(kf, Qs[(c * 2 + s) * 64], acc, 0, 0, 0); }
;             acc = __builtin_amdgcn_mfma_f32_32x32x16_bf16(kx, Qs[(4 + c) * 64], acc, 0, 0, 0);
;             S[kb] = acc;
;         }
;         if (near) {
; #pragma unroll
;             for (int kb = 0; kb < 2; ++kb)
; #pragma unroll
;                 for (int r = 0; r < 16; ++r) S[kb][r] += bm[kb][r]; }
;         float ls = 0.f;
;         bf16x8 Pf[4];
; #pragma unroll
;         for (int kb = 0; kb < 2; ++kb) {
; #pragma unroll
;             for (int r = 0; r < 16; ++r) { const float pv = __builtin_amdgcn_exp2f(S[kb][r]); ls += pv; S[kb][r] = pv; }
; #pragma unroll
;             for (int s = 0; s < 2; ++s) Pf[2 * kb + s] = pack_acc(S[kb], s);
;         }
;         lsum[c] += ls;
; #pragma unroll
;         for (int st = 0; st < 4; ++st)
; #pragma unroll
;             for (int dvb = 0; dvb < 2; ++dvb) O[c][dvb] = __builtin_amdgcn_mfma_f32_32x32x16_bf16(Vf[st][dvb], Pf[st], O[c][dvb], 0, 0, 0);
.LBB0_786:
	s_mul_i32 s0, s57, 0x2400
	v_add_u32_e32 v193, s0, v188
	ds_read_b128 v[66:69], v193 offset:4096
	ds_read_b128 v[70:73], v189 offset:40960
	ds_read_b128 v[110:113], v189 offset:41984
	ds_read_b128 v[194:197], v189 offset:45056
	v_cndmask_b32_e64 v198, 0, 1, s[38:39]
	v_cmp_ne_u32_e64 s[0:1], 1, v198
	s_waitcnt lgkmcnt(2)
	v_mfma_f32_32x32x16_bf16 v[82:97], v[66:69], v[70:73], 0
	ds_read_b128 v[66:69], v193 offset:4128
	ds_read_b128 v[74:77], v193 offset:8704
	ds_read_b128 v[114:117], v193 offset:8736
	ds_read_b128 v[138:141], v193 offset:22528
	ds_read_b128 v[130:133], v193 offset:22560
	ds_read_b128 v[122:125], v193 offset:22592
	s_andn2_b64 vcc, exec, s[38:39]
	s_waitcnt lgkmcnt(5)
	v_mfma_f32_32x32x16_bf16 v[82:97], v[66:69], v[110:113], v[82:97]
	s_waitcnt lgkmcnt(4)
	v_mfma_f32_32x32x16_bf16 v[66:81], v[74:77], v[70:73], 0
	s_waitcnt lgkmcnt(3)
	v_mfma_f32_32x32x16_bf16 v[66:81], v[114:117], v[110:113], v[66:81]
	ds_read_b128 v[126:129], v193 offset:27168
	ds_read_b128 v[118:121], v193 offset:27200
	ds_read_b128 v[134:137], v193 offset:27136
	ds_read_b128 v[114:117], v193 offset:22624
	ds_read_b128 v[110:113], v193 offset:27232
	v_mfma_f32_32x32x16_bf16 v[82:97], v[98:101], v[194:197], v[82:97]
	v_mfma_f32_32x32x16_bf16 v[66:81], v[98:101], v[194:197], v[66:81]
	s_cbranch_vccnz .LBB0_788
	s_nop 9
	v_add_f32_e32 v82, v152, v82
	v_add_f32_e32 v83, v153, v83
	v_add_f32_e32 v84, v154, v84
	v_add_f32_e32 v85, v155, v85
	v_add_f32_e32 v86, v156, v86
	v_add_f32_e32 v87, v157, v87
	v_add_f32_e32 v88, v158, v88
	v_add_f32_e32 v89, v159, v89
	v_add_f32_e32 v90, v160, v90
	v_add_f32_e32 v91, v161, v91
	v_add_f32_e32 v92, v162, v92
	v_add_f32_e32 v93, v163, v93
	v_add_f32_e32 v94, v164, v94
	v_add_f32_e32 v95, v165, v95
	v_add_f32_e32 v96, v166, v96
	v_add_f32_e32 v97, v167, v97
	v_add_f32_e32 v66, v168, v66
	v_add_f32_e32 v67, v169, v67
	v_add_f32_e32 v68, v170, v68
	v_add_f32_e32 v69, v171, v69
	v_add_f32_e32 v70, v172, v70
	v_add_f32_e32 v71, v173, v71
	v_add_f32_e32 v72, v174, v72
	v_add_f32_e32 v73, v175, v73
	v_add_f32_e32 v74, v176, v74
	v_add_f32_e32 v75, v177, v75
	v_add_f32_e32 v76, v178, v76
	v_add_f32_e32 v77, v179, v77
	v_add_f32_e32 v78, v180, v78
	v_add_f32_e32 v79, v181, v79
	v_add_f32_e32 v80, v182, v80
	v_add_f32_e32 v81, v183, v81
.LBB0_788:
	s_nop 9
	v_exp_f32_e32 v194, v82
	v_exp_f32_e32 v195, v83
	v_exp_f32_e32 v196, v84
	v_exp_f32_e32 v197, v85
	v_exp_f32_e32 v198, v86
	v_exp_f32_e32 v199, v87
	v_exp_f32_e32 v223, v88
	v_exp_f32_e32 v224, v89
	v_cvt_pk_bf16_f32 v82, v194, v195
	v_cvt_pk_bf16_f32 v83, v196, v197
	v_cvt_pk_bf16_f32 v84, v198, v199
	v_cvt_pk_bf16_f32 v85, v223, v224
	v_exp_f32_e32 v225, v90
	v_exp_f32_e32 v226, v91
	s_waitcnt lgkmcnt(7)
	v_mfma_f32_32x32x16_bf16 v[50:65], v[138:141], v[82:85], v[50:65]
	v_exp_f32_e32 v227, v92
	v_exp_f32_e32 v228, v93
	v_exp_f32_e32 v229, v94
	v_exp_f32_e32 v230, v95
	v_exp_f32_e32 v231, v96
	v_exp_f32_e32 v232, v97
	v_exp_f32_e32 v233, v66
	s_waitcnt lgkmcnt(2)
	v_mfma_f32_32x32x16_bf16 v[18:33], v[134:137], v[82:85], v[18:33]
	v_cvt_pk_bf16_f32 v82, v225, v226
	v_cvt_pk_bf16_f32 v83, v227, v228
	v_cvt_pk_bf16_f32 v84, v229, v230
	v_cvt_pk_bf16_f32 v85, v231, v232
	v_exp_f32_e32 v234, v67
	v_exp_f32_e32 v235, v68
	v_exp_f32_e32 v236, v69
	v_mfma_f32_32x32x16_bf16 v[50:65], v[130:133], v[82:85], v[50:65]
	v_exp_f32_e32 v237, v70
	v_exp_f32_e32 v238, v71
	v_exp_f32_e32 v239, v72
	v_exp_f32_e32 v240, v73
	v_cvt_pk_bf16_f32 v66, v233, v234
	v_cvt_pk_bf16_f32 v67, v235, v236
	v_cvt_pk_bf16_f32 v68, v237, v238
	v_mfma_f32_32x32x16_bf16 v[18:33], v[126:129], v[82:85], v[18:33]
	v_cvt_pk_bf16_f32 v69, v239, v240
	v_exp_f32_e32 v241, v74
	v_exp_f32_e32 v242, v75
	v_exp_f32_e32 v243, v76
	v_exp_f32_e32 v244, v77
	v_exp_f32_e32 v245, v78
	v_exp_f32_e32 v246, v79
	v_mfma_f32_32x32x16_bf16 v[50:65], v[122:125], v[66:69], v[50:65]
	v_exp_f32_e32 v247, v80
	v_exp_f32_e32 v248, v81
	s_and_b64 vcc, exec, s[0:1]
	v_mfma_f32_32x32x16_bf16 v[18:33], v[118:121], v[66:69], v[18:33]
	v_cvt_pk_bf16_f32 v66, v241, v242
	v_cvt_pk_bf16_f32 v67, v243, v244
	v_cvt_pk_bf16_f32 v68, v245, v246
	v_cvt_pk_bf16_f32 v69, v247, v248
	s_waitcnt lgkmcnt(1)
	s_nop 0
	v_mfma_f32_32x32x16_bf16 v[50:65], v[114:117], v[66:69], v[50:65]
	s_waitcnt lgkmcnt(0)
	v_mfma_f32_32x32x16_bf16 v[18:33], v[110:113], v[66:69], v[18:33]
	ds_read_b128 v[66:69], v193 offset:4160
	ds_read_b128 v[70:73], v189 offset:43008
	ds_read_b128 v[206:209], v189 offset:44032
	ds_read_b128 v[210:213], v189 offset:46080
	s_waitcnt lgkmcnt(2)
	v_mfma_f32_32x32x16_bf16 v[82:97], v[66:69], v[70:73], 0
	ds_read_b128 v[66:69], v193 offset:4192
	ds_read_b128 v[74:77], v193 offset:8768
	ds_read_b128 v[200:203], v193 offset:8800
	s_waitcnt lgkmcnt(2)
	v_mfma_f32_32x32x16_bf16 v[82:97], v[66:69], v[206:209], v[82:97]
	s_waitcnt lgkmcnt(1)
	v_mfma_f32_32x32x16_bf16 v[66:81], v[74:77], v[70:73], 0
	s_waitcnt lgkmcnt(0)
	v_mfma_f32_32x32x16_bf16 v[66:81], v[200:203], v[206:209], v[66:81]
	v_mfma_f32_32x32x16_bf16 v[82:97], v[98:101], v[210:213], v[82:97]
	v_mfma_f32_32x32x16_bf16 v[66:81], v[98:101], v[210:213], v[66:81]
	s_cbranch_vccnz .LBB0_790
	s_nop 9
	v_add_f32_e32 v82, v152, v82
	v_add_f32_e32 v83, v153, v83
	v_add_f32_e32 v84, v154, v84
	v_add_f32_e32 v85, v155, v85
	v_add_f32_e32 v86, v156, v86
	v_add_f32_e32 v87, v157, v87
	v_add_f32_e32 v88, v158, v88
	v_add_f32_e32 v89, v159, v89
	v_add_f32_e32 v90, v160, v90
	v_add_f32_e32 v91, v161, v91
	v_add_f32_e32 v92, v162, v92
	v_add_f32_e32 v93, v163, v93
	v_add_f32_e32 v94, v164, v94
	v_add_f32_e32 v95, v165, v95
	v_add_f32_e32 v96, v166, v96
	v_add_f32_e32 v97, v167, v97
	v_add_f32_e32 v66, v168, v66
	v_add_f32_e32 v67, v169, v67
	v_add_f32_e32 v68, v170, v68
	v_add_f32_e32 v69, v171, v69
	v_add_f32_e32 v70, v172, v70
	v_add_f32_e32 v71, v173, v71
	v_add_f32_e32 v72, v174, v72
	v_add_f32_e32 v73, v175, v73
	v_add_f32_e32 v74, v176, v74
	v_add_f32_e32 v75, v177, v75
	v_add_f32_e32 v76, v178, v76
	v_add_f32_e32 v77, v179, v77
	v_add_f32_e32 v78, v180, v78
	v_add_f32_e32 v79, v181, v79
	v_add_f32_e32 v80, v182, v80
	v_add_f32_e32 v81, v183, v81

; __device__ __forceinline__ float frsq(float x) { return __builtin_amdgcn_rsqf(x); }
; __device__ __forceinline__ int lt_tid(int wv) { int ln; asm volatile("v_mbcnt_lo_u32_b32 %0, -1, 0\n\tv_mbcnt_hi_u32_b32 %0, -1, %0" : "=v"(ln)); return (wv << 6) | ln; }
;     ...
;         const float l0 = lsum[0] + __shfl_xor(lsum[0], 32), l1 = lsum[1] + __shfl_xor(lsum[1], 32);
;         const float i0 = 1.0f / l0, i1 = lam / l1;
;         float ss = 0.f;
; #pragma unroll
;         for (int d = 0; d < 2; ++d)
; #pragma unroll
;             for (int r = 0; r < 16; ++r) { const float o = O[0][d][r] * i0 - O[1][d][r] * i1; O[0][d][r] = o; ss += o * o; }
;         ss += __shfl_xor(ss, 32);
;         const float rn = frsq(ss * (1.f / 64.f) + 1e-5f) * (1.0f - lam_init);
;         const int lane2 = lt_tid(wvid) & 63, qpos2 = q0w + (lane2 & 31), hi2 = lane2 >> 5;
.LBB0_793:
	ds_bpermute_b32 v0, v190, v191
	ds_bpermute_b32 v66, v190, v192
	s_and_b64 s[0:1], s[24:25], exec
	s_waitcnt lgkmcnt(1)
	v_add_f32_e32 v0, v191, v0
	v_div_scale_f32 v67, s[0:1], v0, v0, 1.0
	v_rcp_f32_e32 v68, v67
	s_waitcnt lgkmcnt(0)
	v_add_f32_e32 v66, v192, v66
	v_fma_f32 v69, -v67, v68, 1.0
	v_fmac_f32_e32 v68, v69, v68
	v_div_scale_f32 v69, vcc, 1.0, v0, 1.0
	v_mul_f32_e32 v70, v69, v68
	v_fma_f32 v71, -v67, v70, v69
	v_fmac_f32_e32 v70, v71, v68
	v_fma_f32 v67, -v67, v70, v69
	v_div_fmas_f32 v67, v67, v68, v70
	v_div_fixup_f32 v0, v67, v0, 1.0
	v_div_scale_f32 v67, s[0:1], v66, v66, v184
	v_rcp_f32_e32 v68, v67
	s_cselect_b32 s0, 0x1010, 16
	v_fma_f32 v69, -v67, v68, 1.0
	v_fmac_f32_e32 v68, v69, v68
	v_div_scale_f32 v69, vcc, v184, v66, v184
	v_mul_f32_e32 v70, v69, v68
	v_fma_f32 v71, -v67, v70, v69
	v_fmac_f32_e32 v70, v71, v68
	v_fma_f32 v67, -v67, v70, v69
	v_div_fmas_f32 v67, v67, v68, v70
	v_div_fixup_f32 v70, v67, v66, v184
	v_mul_f32_e32 v34, v34, v70
	v_mul_f32_e32 v35, v35, v70
	v_mul_f32_e32 v2, v2, v70
	v_mul_f32_e32 v3, v3, v70
	v_fma_f32 v66, v50, v0, -v34
	v_fma_f32 v67, v51, v0, -v35
	v_mul_f32_e32 v34, v36, v70
	v_mul_f32_e32 v35, v37, v70
	v_fma_f32 v36, v18, v0, -v2
	v_fma_f32 v37, v19, v0, -v3
	v_fma_f32 v68, v52, v0, -v34
	v_fma_f32 v69, v53, v0, -v35
	v_mul_f32_e32 v34, v38, v70
	v_mul_f32_e32 v35, v39, v70
	v_mul_f32_e32 v2, v4, v70
	v_mul_f32_e32 v3, v5, v70
	v_fma_f32 v54, v54, v0, -v34
	v_fma_f32 v55, v55, v0, -v35
	v_mul_f32_e32 v34, v40, v70
	v_mul_f32_e32 v35, v41, v70
	v_mul_f32_e32 v72, v66, v66
	v_mul_f32_e32 v73, v67, v67
	v_fma_f32 v52, v56, v0, -v34
	v_fma_f32 v53, v57, v0, -v35
	v_mul_f32_e32 v34, v42, v70
	v_mul_f32_e32 v35, v43, v70
	v_mul_f32_e32 v74, v68, v68
	v_mul_f32_e32 v75, v69, v69
	v_fma_f32 v50, v58, v0, -v34
	v_fma_f32 v51, v59, v0, -v35
	v_mul_f32_e32 v34, v44, v70
	v_mul_f32_e32 v35, v45, v70
	v_mul_f32_e32 v76, v54, v54
	v_mul_f32_e32 v77, v55, v55
	v_fma_f32 v42, v60, v0, -v34
	v_fma_f32 v43, v61, v0, -v35
	v_mul_f32_e32 v34, v46, v70
	v_mul_f32_e32 v35, v47, v70
	v_mul_f32_e32 v56, v52, v52
	v_mul_f32_e32 v57, v53, v53
	v_fma_f32 v40, v62, v0, -v34
	v_fma_f32 v41, v63, v0, -v35
	v_mul_f32_e32 v34, v48, v70
	v_mul_f32_e32 v35, v49, v70
	v_mul_f32_e32 v58, v50, v50
	v_mul_f32_e32 v59, v51, v51
	v_fma_f32 v38, v64, v0, -v34
	v_fma_f32 v39, v65, v0, -v35
	v_fma_f32 v34, v20, v0, -v2
	v_fma_f32 v35, v21, v0, -v3
	v_mul_f32_e32 v2, v6, v70
	v_mul_f32_e32 v3, v7, v70
	v_mul_f32_e32 v44, v42, v42
	v_mul_f32_e32 v45, v43, v43
	v_fma_f32 v20, v22, v0, -v2
	v_fma_f32 v21, v23, v0, -v3
	v_mul_f32_e32 v2, v8, v70
	v_mul_f32_e32 v3, v9, v70
	v_mul_f32_e32 v46, v40, v40
	v_mul_f32_e32 v47, v41, v41
	v_fma_f32 v18, v24, v0, -v2
	v_fma_f32 v19, v25, v0, -v3
	v_mul_f32_e32 v2, v10, v70
	v_mul_f32_e32 v3, v11, v70
	v_mul_f32_e32 v48, v38, v38
	v_mul_f32_e32 v49, v39, v39
	v_fma_f32 v8, v26, v0, -v2
	v_fma_f32 v9, v27, v0, -v3
	v_mul_f32_e32 v2, v12, v70
	v_mul_f32_e32 v3, v13, v70
	v_mul_f32_e32 v60, v36, v36
	v_mul_f32_e32 v61, v37, v37
	v_fma_f32 v6, v28, v0, -v2
	v_fma_f32 v7, v29, v0, -v3
	v_mul_f32_e32 v2, v14, v70
	v_mul_f32_e32 v3, v15, v70
	v_mul_f32_e32 v62, v34, v34
	v_mul_f32_e32 v63, v35, v35
	v_fma_f32 v4, v30, v0, -v2
	v_fma_f32 v5, v31, v0, -v3
	v_mul_f32_e32 v2, v16, v70
	v_mul_f32_e32 v3, v17, v70
	v_mul_f32_e32 v22, v20, v20
	v_mul_f32_e32 v23, v21, v21
	v_fma_f32 v2, v32, v0, -v2
	v_fma_f32 v3, v33, v0, -v3
	v_add_f32_e32 v0, v72, v73
	v_add_f32_e32 v0, v74, v0
	v_add_f32_e32 v0, v75, v0
	v_add_f32_e32 v0, v76, v0
	v_add_f32_e32 v0, v77, v0
	v_add_f32_e32 v0, v56, v0
	v_add_f32_e32 v0, v57, v0
	v_add_f32_e32 v0, v58, v0
	v_add_f32_e32 v0, v59, v0
	v_add_f32_e32 v0, v44, v0
	v_add_f32_e32 v0, v45, v0
	v_add_f32_e32 v0, v46, v0
	v_add_f32_e32 v0, v47, v0
	v_add_f32_e32 v0, v48, v0
	v_add_f32_e32 v0, v49, v0
	v_add_f32_e32 v0, v60, v0
	v_add_f32_e32 v0, v61, v0
	v_add_f32_e32 v0, v62, v0
	v_add_f32_e32 v0, v63, v0
	v_add_f32_e32 v0, v22, v0
	v_mul_f32_e32 v24, v18, v18
	v_mul_f32_e32 v25, v19, v19
	v_add_f32_e32 v0, v23, v0
	v_add_f32_e32 v0, v24, v0
	v_mul_f32_e32 v10, v8, v8
	v_mul_f32_e32 v11, v9, v9
	v_add_f32_e32 v0, v25, v0
	v_add_f32_e32 v0, v10, v0
	v_mul_f32_e32 v12, v6, v6
	v_mul_f32_e32 v13, v7, v7
	v_add_f32_e32 v0, v11, v0
	v_add_f32_e32 v0, v12, v0
	v_mul_f32_e32 v14, v4, v4
	v_mul_f32_e32 v15, v5, v5
	v_add_f32_e32 v0, v13, v0
	v_add_f32_e32 v0, v14, v0
	v_mul_f32_e32 v16, v2, v2
	v_mul_f32_e32 v17, v3, v3
	v_add_f32_e32 v0, v15, v0
	v_add_f32_e32 v0, v16, v0
	v_add_f32_e32 v10, v17, v0
	ds_bpermute_b32 v11, v190, v10
	v_mbcnt_lo_u32_b32 v0, -1, 0
	v_mbcnt_hi_u32_b32 v0, -1, v0
	s_nop 0
	v_and_b32_e32 v12, 31, v0
	v_add_u32_e32 v12, s49, v12
	v_cmp_gt_i32_e32 vcc, s0, v12
	s_and_b64 s[0:1], s[28:29], vcc
	s_and_saveexec_b64 s[24:25], s[0:1]
	s_xor_b64 s[0:1], exec, s[24:25]
	s_cbranch_execz .LBB0_768
; __device__ __forceinline__ float frsq(float x) { return __builtin_amdgcn_rsqf(x); }
; __device__ __forceinline__ int lt_tid(int wv) { int ln; asm volatile("v_mbcnt_lo_u32_b32 %0, -1, 0\n\tv_mbcnt_hi_u32_b32 %0, -1, %0" : "=v"(ln)); return (wv << 6) | ln; }
; __device__ __forceinline__ unsigned pkbf(float lo, float hi) { f32x2_t v = {lo, hi}; bf16x2_t b = __builtin_convertvector(v, bf16x2_t); return __builtin_bit_cast(unsigned, b); }
;     ...
;         const float rn = frsq(ss * (1.f / 64.f) + 1e-5f) * (1.0f - lam_init);
;         const int lane2 = lt_tid(wvid) & 63, qpos2 = q0w + (lane2 & 31), hi2 = lane2 >> 5;
;         if (wave_on && qpos2 < LT && (qi > 0 || qpos2 < NMETA)) {
;             bf16_t* orow = MIX + ((size_t)b * LT + qpos2) * D + M_B + h * 64;
; #pragma unroll
;             for (int d = 0; d < 2; ++d)
; #pragma unroll
;                 for (int g4 = 0; g4 < 4; ++g4) { const int dv0 = 32 * d + 8 * g4 + 4 * hi2; const f32x4 gg = *(const f32x4*)(p.in[I_SUBLN] + l * 64 + dv0);
;                     u32x2 w; w.x = pkbf(O[0][d][4 * g4] * rn * gg[0], O[0][d][4 * g4 + 1] * rn * gg[1]); w.y = pkbf(O[0][d][4 * g4 + 2] * rn * gg[2], O[0][d][4 * g4 + 3] * rn * gg[3]);
;                     *(u32x2*)(orow + dv0) = w; }
	v_ashrrev_i32_e32 v13, 31, v12
	v_lshl_add_u64 v[12:13], v[12:13], 0, s[22:23]
	v_lshrrev_b32_e32 v0, 3, v0
	v_lshlrev_b64 v[12:13], 11, v[12:13]
	v_and_b32_e32 v0, 4, v0
	s_waitcnt lgkmcnt(0)
	v_add_f32_e32 v10, v10, v11
	v_lshl_add_u64 v[12:13], s[6:7], 0, v[12:13]
	v_lshlrev_b32_e32 v11, 2, v0
	v_lshl_add_u64 v[16:17], v[12:13], 0, s[40:41]
	global_load_dwordx4 v[12:15], v11, s[20:21]
	global_load_dwordx4 v[114:117], v11, s[20:21] offset:32
	global_load_dwordx4 v[118:121], v11, s[20:21] offset:64
	global_load_dwordx4 v[122:125], v11, s[20:21] offset:96
	global_load_dwordx4 v[126:129], v11, s[20:21] offset:128
	global_load_dwordx4 v[130:133], v11, s[20:21] offset:160
	global_load_dwordx4 v[134:137], v11, s[20:21] offset:192
	global_load_dwordx4 v[138:141], v11, s[20:21] offset:224
	v_fmamk_f32 v10, v10, 0x3c800000, v204
	v_rsq_f32_e32 v10, v10
	v_lshlrev_b32_e32 v0, 1, v0
	s_mov_b64 s[22:23], 0xf1f0200
	v_mul_f32_e32 v10, v187, v10
	v_mul_f32_e32 v22, v66, v10
	v_mul_f32_e32 v23, v67, v10
	v_mul_f32_e32 v20, v20, v10
	v_mul_f32_e32 v21, v21, v10
	v_mul_f32_e32 v18, v18, v10
	v_mul_f32_e32 v19, v19, v10
	v_mul_f32_e32 v8, v8, v10
	v_mul_f32_e32 v9, v9, v10
	v_mul_f32_e32 v6, v6, v10
	v_mul_f32_e32 v7, v7, v10
	v_mul_f32_e32 v4, v4, v10
	v_mul_f32_e32 v5, v5, v10
	v_mul_f32_e32 v2, v2, v10
	v_mul_f32_e32 v3, v3, v10
	s_waitcnt vmcnt(0)
	v_mul_f32_e32 v12, v22, v12
	v_mul_f32_e32 v13, v23, v13
	s_nop 0
	v_cvt_pk_bf16_f32 v22, v12, v13
	v_mul_f32_e32 v12, v68, v10
	v_mul_f32_e32 v13, v69, v10
	s_nop 0
	v_mul_f32_e32 v12, v12, v14
	v_mul_f32_e32 v13, v13, v15
	v_lshl_add_u64 v[14:15], v[16:17], 0, v[0:1]
	v_cvt_pk_bf16_f32 v23, v12, v13
	v_lshl_add_u64 v[12:13], v[14:15], 0, s[22:23]
	s_mov_b32 s22, 0xf1f0000
	v_add_co_u32_e32 v14, vcc, s22, v14
	s_nop 1
	v_addc_co_u32_e32 v15, vcc, 0, v15, vcc
	global_store_dwordx2 v[14:15], v[22:23], off offset:512
	s_nop 1
	v_mov_b64_e32 v[14:15], v[114:115]
	v_mov_b64_e32 v[16:17], v[116:117]
	v_mul_f32_e32 v22, v54, v10
	v_mul_f32_e32 v23, v55, v10
	v_mul_f32_e32 v14, v22, v14
	v_mul_f32_e32 v15, v23, v15
	v_mul_f32_e32 v22, v52, v10
	v_mul_f32_e32 v23, v53, v10
	v_cvt_pk_bf16_f32 v14, v14, v15
	v_mul_f32_e32 v16, v22, v16
	v_mul_f32_e32 v17, v23, v17
	v_mul_f32_e32 v22, v50, v10
	v_mul_f32_e32 v23, v51, v10
	v_cvt_pk_bf16_f32 v15, v16, v17
	global_store_dwordx2 v[12:13], v[14:15], off offset:16
	s_nop 1
	v_mov_b64_e32 v[14:15], v[118:119]
	v_mov_b64_e32 v[16:17], v[120:121]
	v_mul_f32_e32 v14, v22, v14
	v_mul_f32_e32 v15, v23, v15
	v_mul_f32_e32 v22, v42, v10
	v_mul_f32_e32 v23, v43, v10
	v_cvt_pk_bf16_f32 v14, v14, v15
	v_mul_f32_e32 v16, v22, v16
	v_mul_f32_e32 v17, v23, v17
	v_mul_f32_e32 v22, v40, v10
	v_mul_f32_e32 v23, v41, v10
	v_cvt_pk_bf16_f32 v15, v16, v17
	global_store_dwordx2 v[12:13], v[14:15], off offset:32
	s_nop 1
	v_mov_b64_e32 v[14:15], v[122:123]
	v_mov_b64_e32 v[16:17], v[124:125]
	v_mul_f32_e32 v14, v22, v14
	v_mul_f32_e32 v15, v23, v15
	v_mul_f32_e32 v22, v38, v10
	v_mul_f32_e32 v23, v39, v10
	v_cvt_pk_bf16_f32 v14, v14, v15
	v_mul_f32_e32 v16, v22, v16
	v_mul_f32_e32 v17, v23, v17
	v_mul_f32_e32 v22, v36, v10
	v_mul_f32_e32 v23, v37, v10
	v_cvt_pk_bf16_f32 v15, v16, v17
	global_store_dwordx2 v[12:13], v[14:15], off offset:48
	s_nop 1
	v_mov_b64_e32 v[14:15], v[126:127]
	v_mov_b64_e32 v[16:17], v[128:129]
	v_mul_f32_e32 v14, v22, v14
	v_mul_f32_e32 v15, v23, v15
	v_mul_f32_e32 v22, v34, v10
	v_mul_f32_e32 v23, v35, v10
	v_cvt_pk_bf16_f32 v14, v14, v15
	v_mul_f32_e32 v16, v22, v16
	v_mul_f32_e32 v17, v23, v17
	s_nop 0
	v_cvt_pk_bf16_f32 v15, v16, v17
	global_store_dwordx2 v[12:13], v[14:15], off offset:64
	s_nop 1
	v_mov_b64_e32 v[14:15], v[130:131]
	v_mov_b64_e32 v[16:17], v[132:133]
	v_mul_f32_e32 v14, v20, v14
	v_mul_f32_e32 v15, v21, v15
	v_mul_f32_e32 v16, v18, v16
	v_mul_f32_e32 v17, v19, v17
	v_cvt_pk_bf16_f32 v14, v14, v15
	v_cvt_pk_bf16_f32 v15, v16, v17
	global_store_dwordx2 v[12:13], v[14:15], off offset:80
	s_nop 1
	v_mov_b64_e32 v[14:15], v[134:135]
	v_mov_b64_e32 v[16:17], v[136:137]
	v_mul_f32_e32 v8, v8, v14
	v_mul_f32_e32 v9, v9, v15
	v_mul_f32_e32 v6, v6, v16
	v_mul_f32_e32 v7, v7, v17
	v_cvt_pk_bf16_f32 v8, v8, v9
	v_cvt_pk_bf16_f32 v9, v6, v7
	global_store_dwordx2 v[12:13], v[8:9], off offset:96
	s_nop 1
	v_mov_b64_e32 v[6:7], v[138:139]
	v_mov_b64_e32 v[8:9], v[140:141]
	v_mul_f32_e32 v4, v4, v6
	v_mul_f32_e32 v5, v5, v7
	v_mul_f32_e32 v2, v2, v8
	v_mul_f32_e32 v3, v3, v9
	v_cvt_pk_bf16_f32 v4, v4, v5
	v_cvt_pk_bf16_f32 v5, v2, v3
	global_store_dwordx2 v[12:13], v[4:5], off offset:112
	s_branch .LBB0_768

; __device__ __forceinline__ float bflo(unsigned w) { return __uint_as_float(w << 16); }
; __device__ __forceinline__ float bfhi(unsigned w) { return __uint_as_float(w & 0xFFFF0000u); }
; __device__ __forceinline__ unsigned pkbf(float lo, float hi) { f32x2_t v = {lo, hi}; bf16x2_t b = __builtin_convertvector(v, bf16x2_t); return __builtin_bit_cast(unsigned, b); }
;     ...
;         const int u = *ucur;
;         if (u >= 33 * 16) break;
;         const int qi = 32 - u / 16, bk = u % 16, b = bk >> 1, hkv = bk & 1, hq = 2 * hkv + (wave >> 2);
;         const int q0 = qi == 0 ? 0 : 16 + 128 * (qi - 1);
;         const int ktlo = max(1, (q0 - 127) / 64), kthi = qi == 0 ? 0 : (q0 + 127) / 64;
;         const int ntile = 1 + (kthi >= ktlo ? kthi - ktlo + 1 : 0);
;         const int q0w = q0 + 32 * (wave & 3), qpos = q0w + l31;
;         const bool wave_on = (qi > 0) || ((wave & 3) == 0);
;         const size_t qrow = (size_t)b * LT + (qpos < LT ? qpos : LT - 1);
;         bf16x8 Qf[4]; bf16x8 qx; float lsum;
;         { u32x4 qraw[4]; float qn2 = 0.f;
; #pragma unroll
;           for (int s = 0; s < 4; ++s) qraw[s] = *(const u32x4*)(U + qrow * INW + C_QA + hq * 64 + s * 16 + hi * 8);
;           const float km2 = __uint_as_float(__hip_atomic_load((const unsigned*)(ws + WS_CTL) + CW_KMX + l * 256 + 128 + b * 2 + hkv, __ATOMIC_RELAXED, __HIP_MEMORY_SCOPE_AGENT));
; #pragma unroll
;           for (int s = 0; s < 4; ++s) { const unsigned qw[4] = {qraw[s].x, qraw[s].y, qraw[s].z, qraw[s].w}; u32x4 qs;
; #pragma unroll
;               for (int e = 0; e < 4; ++e) qn2 += bflo(qw[e]) * bflo(qw[e]) + bfhi(qw[e]) * bfhi(qw[e]);
;               qs.x = pkbf(bflo(qw[0]) * c2, bfhi(qw[0]) * c2); qs.y = pkbf(bflo(qw[1]) * c2, bfhi(qw[1]) * c2); qs.z = pkbf(bflo(qw[2]) * c2, bfhi(qw[2]) * c2); qs.w = pkbf(bflo(qw[3]) * c2, bfhi(qw[3]) * c2);
;               Qf[s] = __builtin_bit_cast(bf16x8, qs); }
;           qn2 += __shfl_xor(qn2, 32);
.LBB0_814:
	v_add_u32_e32 v2, v0, v2
	v_and_b32_e32 v2, -16, v2
	v_sub_u32_e32 v8, v0, v2
	v_and_b32_e32 v11, 1, v8
	v_lshlrev_b32_e32 v2, 1, v11
	s_waitcnt vmcnt(0)
	v_add_u32_e32 v76, s34, v2
	v_add_u32_e32 v2, 0xffffff81, v50
	v_ashrrev_i32_e32 v3, 31, v2
	v_lshrrev_b32_e32 v3, 26, v3
	v_add_u32_e32 v2, v2, v3
	v_ashrrev_i32_e32 v2, 6, v2
	v_max_i32_e32 v51, 1, v2
	v_add_u32_e32 v2, 0x7f, v50
	v_lshrrev_b32_e32 v2, 6, v2
	v_cndmask_b32_e64 v2, v2, 0, s[0:1]
	v_sub_co_u32_e32 v2, vcc, v2, v51
	v_lshrrev_b32_e32 v41, 1, v8
	v_readfirstlane_b32 s0, v2
	v_add_u32_e32 v120, s35, v50
	s_add_i32 s8, s0, 2
	v_add_u32_e32 v40, v120, v112
	s_movk_i32 s0, 0x200
	v_mul_lo_u32 v104, v41, s33
	v_cmp_gt_i32_e64 s[6:7], s0, v0
	v_ashrrev_i32_e32 v105, 31, v104
	v_min_i32_e32 v0, 0x100f, v40
	v_lshl_add_u64 v[2:3], v[0:1], 0, v[104:105]
	v_mov_b64_e32 v[4:5], s[16:17]
	v_mad_u64_u32 v[4:5], s[0:1], v2, s97, v[4:5]
	s_waitcnt vmcnt(0)
	v_lshlrev_b32_e32 v106, 6, v76
	v_mad_i32_i24 v5, v3, s97, v5
	v_ashrrev_i32_e32 v107, 31, v106
	v_lshl_add_u64 v[2:3], v[106:107], 1, v[4:5]
	v_mov_b32_e32 v103, v1
	v_lshl_add_u64 v[6:7], v[2:3], 0, v[102:103]
	global_load_dwordx4 v[2:5], v[6:7], off
	global_load_dwordx4 v[12:15], v[6:7], off offset:32
	global_load_dwordx4 v[42:45], v[6:7], off offset:64
	global_load_dwordx4 v[46:49], v[6:7], off offset:96
	v_and_b32_e32 v6, -2, v8
	v_ashrrev_i32_e32 v7, 31, v6
	v_lshlrev_b64 v[6:7], 2, v[6:7]
	s_and_b64 s[0:1], vcc, exec
	v_lshl_add_u64 v[6:7], s[26:27], 0, v[6:7]
	v_lshlrev_b32_e32 v0, 2, v11
	v_readfirstlane_b32 s1, v7
	v_readfirstlane_b32 s0, v6
	v_readlane_b32 s48, v253, 12
	v_readlane_b32 s58, v253, 22
	v_readlane_b32 s59, v253, 23
	s_cselect_b32 s37, 1, s8
	s_or_b64 s[28:29], s[6:7], s[24:25]
	global_load_dword v0, v0, s[0:1] sc1
	s_mov_b32 s0, 0xf800000
	s_cmp_lt_i32 s37, 1
	v_add_u32_e32 v144, s36, v76
	v_ashrrev_i32_e32 v145, 31, v144
	v_lshlrev_b64 v[144:145], 2, v[144:145]
	s_mov_b32 s30, 0x1616000
	v_mul_lo_u32 v148, v41, s30
	v_mul_hi_i32 v149, v104, s97
	v_lshl_add_u64 v[144:145], s[58:59], 0, v[144:145]
	global_load_dword v146, v[144:145], off
	v_lshl_add_u64 v[148:149], s[16:17], 0, v[148:149]
	v_lshlrev_b32_e32 v150, 7, v11
	v_mov_b32_e32 v151, 0
	v_lshl_add_u64 v[128:129], v[148:149], 0, v[150:151]
	s_mov_b32 s30, 0x41000
	v_mul_lo_u32 v148, v8, s30
	v_ashrrev_i32_e32 v149, 31, v148
	v_lshlrev_b64 v[148:149], 1, v[148:149]
	v_lshl_add_u64 v[130:131], s[18:19], 0, v[148:149]
	v_lshl_add_u64 v[148:149], v[98:99], 1, v[128:129]
	global_load_dwordx4 v[136:139], v[148:149], off offset:512
	v_lshl_add_u64 v[148:149], v[100:101], 1, v[130:131]
	global_load_dwordx4 v[140:143], v[148:149], off
	v_readlane_b32 s49, v253, 13
	v_readlane_b32 s50, v253, 14
	v_readlane_b32 s51, v253, 15
	v_readlane_b32 s52, v253, 16
	v_readlane_b32 s53, v253, 17
	v_readlane_b32 s54, v253, 18
	v_readlane_b32 s55, v253, 19
	v_readlane_b32 s56, v253, 20
	v_readlane_b32 s57, v253, 21
	v_readlane_b32 s60, v253, 24
	v_readlane_b32 s61, v253, 25
	v_readlane_b32 s62, v253, 26
	v_readlane_b32 s63, v253, 27
	s_waitcnt vmcnt(7)
	v_lshlrev_b32_e32 v20, 16, v2
	v_and_b32_e32 v21, 0xffff0000, v2
	v_lshlrev_b32_e32 v26, 16, v3
	s_waitcnt vmcnt(4)
	v_and_b32_e32 v7, 0xffff0000, v47
	v_and_b32_e32 v27, 0xffff0000, v3
	v_lshlrev_b32_e32 v30, 16, v14
	v_and_b32_e32 v31, 0xffff0000, v14
	v_lshlrev_b32_e32 v36, 16, v15
	v_and_b32_e32 v37, 0xffff0000, v15
	v_lshlrev_b32_e32 v10, 16, v46
	v_and_b32_e32 v15, 0xffff0000, v46
	v_mov_b32_e32 v14, v7
	v_and_b32_e32 v9, 0xffff0000, v49
	v_mul_f32_e32 v52, v20, v20
	v_mul_f32_e32 v53, v21, v21
	v_mul_f32_e32 v54, v26, v26
	v_mul_f32_e32 v55, v27, v27
	v_lshlrev_b32_e32 v32, 16, v4
	v_and_b32_e32 v33, 0xffff0000, v4
	v_lshlrev_b32_e32 v38, 16, v5
	v_and_b32_e32 v39, 0xffff0000, v5
	v_lshlrev_b32_e32 v18, 16, v12
	v_and_b32_e32 v19, 0xffff0000, v12
	v_lshlrev_b32_e32 v24, 16, v13
	v_and_b32_e32 v25, 0xffff0000, v13
	v_lshlrev_b32_e32 v4, 16, v47
	v_mov_b32_e32 v5, v10
	v_mul_f32_e32 v2, v14, v14
	v_mul_f32_e32 v3, v15, v15
	v_and_b32_e32 v13, 0xffff0000, v48
	v_mov_b32_e32 v12, v9
	v_mul_f32_e32 v56, v32, v32
	v_mul_f32_e32 v57, v33, v33
	v_fma_f32 v46, v4, v4, v2
	v_fma_f32 v47, v5, v5, v3
	v_lshlrev_b32_e32 v6, 16, v48
	v_lshlrev_b32_e32 v2, 16, v49
	v_mul_f32_e32 v48, v12, v12
	v_mul_f32_e32 v49, v13, v13
	v_add_f32_e32 v5, v54, v55
	v_add_f32_e32 v12, v52, v53
	v_mul_f32_e32 v58, v38, v38
	v_mul_f32_e32 v59, v39, v39
	v_mov_b32_e32 v3, v6
	v_add_f32_e32 v5, v12, v5
	v_add_f32_e32 v12, v56, v57
	v_mul_f32_e32 v60, v18, v18
	v_mul_f32_e32 v61, v19, v19
	v_fma_f32 v48, v2, v2, v48
	v_fma_f32 v49, v3, v3, v49
	v_add_f32_e32 v3, v58, v59
	v_add_f32_e32 v5, v12, v5
	v_mul_f32_e32 v62, v24, v24
	v_mul_f32_e32 v63, v25, v25
	v_add_f32_e32 v3, v3, v5
	v_add_f32_e32 v5, v60, v61
	v_mul_f32_e32 v64, v30, v30
	v_mul_f32_e32 v65, v31, v31
	v_add_f32_e32 v3, v5, v3
	v_add_f32_e32 v5, v62, v63
	v_mul_f32_e32 v70, v36, v36
	v_mul_f32_e32 v71, v37, v37
	v_lshlrev_b32_e32 v16, 16, v42
	v_and_b32_e32 v17, 0xffff0000, v42
	v_add_f32_e32 v3, v5, v3
	v_add_f32_e32 v5, v64, v65
	v_mul_f32_e32 v72, v16, v16
	v_mul_f32_e32 v73, v17, v17
	v_lshlrev_b32_e32 v22, 16, v43
	v_and_b32_e32 v23, 0xffff0000, v43
	v_add_f32_e32 v3, v5, v3
	v_add_f32_e32 v5, v70, v71
	v_mul_f32_e32 v42, v22, v22
	v_mul_f32_e32 v43, v23, v23
	v_lshlrev_b32_e32 v28, 16, v44
	v_and_b32_e32 v29, 0xffff0000, v44
	v_add_f32_e32 v3, v5, v3
	v_add_f32_e32 v5, v72, v73
	v_mul_f32_e32 v74, v28, v28
	v_mul_f32_e32 v75, v29, v29
	v_lshlrev_b32_e32 v34, 16, v45
	v_and_b32_e32 v35, 0xffff0000, v45
	v_add_f32_e32 v3, v5, v3
	v_add_f32_e32 v5, v42, v43
	v_mul_f32_e32 v44, v34, v34
	v_mul_f32_e32 v45, v35, v35
	v_add_f32_e32 v3, v5, v3
	v_add_f32_e32 v5, v74, v75
	v_add_f32_e32 v3, v5, v3
	v_add_f32_e32 v5, v44, v45
	v_add_f32_e32 v3, v5, v3
	v_and_b32_e32 v12, 64, v222
	v_add_f32_e32 v3, v47, v3
	v_xor_b32_e32 v5, 32, v222
	v_add_u32_e32 v12, 64, v12
	v_add_f32_e32 v3, v46, v3
	v_cmp_lt_i32_e32 vcc, v5, v12
	v_add_f32_e32 v3, v49, v3
	v_add_f32_e32 v3, v48, v3
	v_cndmask_b32_e32 v5, v222, v5, vcc
	v_lshlrev_b32_e32 v103, 2, v5
	ds_bpermute_b32 v5, v103, v3
	v_add_u32_e32 v42, s36, v76
	v_ashrrev_i32_e32 v43, 31, v42
	v_lshlrev_b64 v[42:43], 2, v[42:43]
	v_lshl_add_u64 v[42:43], s[58:59], 0, v[42:43]
	s_waitcnt lgkmcnt(0)
; #define LAS __attribute__((address_space(3)))
; __device__ __forceinline__ float bflo(unsigned w) { return __uint_as_float(w << 16); }
; __device__ __forceinline__ float bfhi(unsigned w) { return __uint_as_float(w & 0xFFFF0000u); }
;     ...
;           for (int s = 0; s < 4; ++s) { const unsigned qw[4] = {qraw[s].x, qraw[s].y, qraw[s].z, qraw[s].w}; u32x4 qs;
; #pragma unroll
;               for (int e = 0; e < 4; ++e) qn2 += bflo(qw[e]) * bflo(qw[e]) + bfhi(qw[e]) * bfhi(qw[e]);
;               qs.x = pkbf(bflo(qw[0]) * c2, bfhi(qw[0]) * c2); qs.y = pkbf(bflo(qw[1]) * c2, bfhi(qw[1]) * c2); qs.z = pkbf(bflo(qw[2]) * c2, bfhi(qw[2]) * c2); qs.w = pkbf(bflo(qw[3]) * c2, bfhi(qw[3]) * c2);
;               Qf[s] = __builtin_bit_cast(bf16x8, qs); }
;           qn2 += __shfl_xor(qn2, 32);
;           const float snk = p.in[I_SINKS][l * 4 + hq] * LOG2E;
;           const float mref = fmaxf(sqrtf(qn2 * km2) * 1.001f * c2 + btab[hq * 132 + 131], snk);
;           u32x4 qxw; qxw.x = hi ? 0u : (pkbf(-mref, 0.f) & 0xffffu); qxw.y = 0u; qxw.z = 0u; qxw.w = 0u; qx = __builtin_bit_cast(bf16x8, qxw);
;           const float mrb = bflo(pkbf(-mref, 0.f));
;           lsum = hi == 0 ? __builtin_amdgcn_exp2f(snk + mrb) : 0.0f; }
;         f32x16 O[2];
; #pragma unroll
;         for (int d = 0; d < 2; ++d)
; #pragma unroll
;             for (int r = 0; r < 16; ++r) O[d][r] = 0.f;
;         const bf16_t* kbase = U + (size_t)b * LT * INW + C_KA + hkv * 64;
;         const bf16_t* vbase = VT + (size_t)bk * 64 * LTP;
;         const unsigned koff = (unsigned)(krow * INW + kch * 8), voff = (unsigned)(krow * LTP + kch * 8);
;         u32x4 kreg = *(const u32x4*)(kbase + koff), vreg = *(const u32x4*)(vbase + voff);
;         *(LAS u32x4*)(KV + krow * DF_PITCH + kch * 16) = kreg; *(LAS u32x4*)(KV + 2 * DF_KB + krow * DF_PITCH + kch * 16) = vreg;
;         __syncthreads();
;         for (int ti = 0; ti < ntile; ++ti) {
;             const int kt = ti == 0 ? 0 : ktlo + ti - 1, k0 = kt * 64, cur = ti & 1;
;             if (ti + 1 < ntile) { const int kn = (ktlo + ti) * 64; kreg = *(const u32x4*)(kbase + (koff + (unsigned)(kn * INW))); vreg = *(const u32x4*)(vbase + (voff + (unsigned)kn)); }
;             if (wave_on && (kt == 0 || (k0 <= q0w + 31 && k0 + 63 >= q0w - 127)))
;                 swa_tile(KV + cur * DF_KB, KV + (2 + cur) * DF_KB, btab + hq * 132, Qf, qx, O, lsum, qpos, k0, l31, hi);
	v_add_f32_e32 v3, v3, v5
	s_nop 0
	s_waitcnt vmcnt(3)
	v_mul_f32_e32 v0, v3, v0
	v_cmp_gt_f32_e32 vcc, s0, v0
	v_mul_f32_e32 v3, 0x4f800000, v0
	v_mul_hi_i32 v43, v104, s97
	v_cndmask_b32_e32 v0, v0, v3, vcc
	v_sqrt_f32_e32 v3, v0
	s_nop 0
	v_add_u32_e32 v12, -1, v3
	v_fma_f32 v14, -v12, v3, v0
	v_cmp_ge_f32_e64 s[0:1], 0, v14
	v_add_u32_e32 v14, 1, v3
	s_nop 0
	v_cndmask_b32_e64 v12, v3, v12, s[0:1]
	v_fma_f32 v3, -v14, v3, v0
	v_cmp_lt_f32_e64 s[0:1], 0, v3
	s_nop 1
	v_cndmask_b32_e64 v3, v12, v14, s[0:1]
	v_mul_f32_e32 v12, 0x37800000, v3
	v_cndmask_b32_e32 v3, v3, v12, vcc
	v_cmp_class_f32_e32 vcc, v0, v250
	s_movk_i32 s0, 0x210
	s_nop 0
	v_cndmask_b32_e32 v0, v3, v0, vcc
	v_mul_lo_u32 v3, v76, s0
	v_add_u32_e32 v122, 0, v3
	ds_read_b32 v3, v122 offset:524
	v_mul_f32_e32 v0, 0x3f8020c5, v0
	s_mov_b32 s0, 0x1616000
	v_mul_lo_u32 v42, v41, s0
	v_lshl_add_u64 v[42:43], s[16:17], 0, v[42:43]
	s_waitcnt lgkmcnt(0)
	v_fmac_f32_e32 v3, 0x3e38aa3b, v0
	s_mov_b32 s0, 0x41000
	s_waitcnt vmcnt(2)
	v_mov_b32_e32 v5, v146
	v_mul_f32_e32 v0, 0xbfb8aa3b, v5
	v_min_f32_e64 v0, -v3, v0
	v_cvt_pk_bf16_f32 v3, v0, 0
	v_lshlrev_b32_e32 v0, 16, v3
	v_fmac_f32_e32 v0, 0x3fb8aa3b, v5
	v_exp_f32_e32 v0, v0
	s_nop 0
	v_cndmask_b32_e64 v121, 0, v0, s[4:5]
	v_lshlrev_b32_e32 v0, 7, v11
	v_lshl_add_u64 v[108:109], v[42:43], 0, v[0:1]
	v_mul_lo_u32 v42, v8, s0
	v_ashrrev_i32_e32 v43, 31, v42
	v_lshlrev_b64 v[42:43], 1, v[42:43]
	v_lshl_add_u64 v[110:111], s[18:19], 0, v[42:43]
	v_lshl_add_u64 v[42:43], v[98:99], 1, v[108:109]
	s_nop 0
	v_lshl_add_u64 v[42:43], v[100:101], 1, v[110:111]
	s_nop 0
	s_waitcnt vmcnt(1)
	ds_write_b128 v113, v[136:139] offset:8192
	s_waitcnt vmcnt(0)
	ds_write_b128 v113, v[140:143] offset:26624
	s_waitcnt lgkmcnt(0)
	s_barrier
	s_cbranch_scc1 .LBB0_819
	s_cmp_lg_u32 s37, 1
	s_mov_b32 s0, 0x2c000
	s_cselect_b64 s[30:31], -1, 0
	s_cmp_eq_u32 s37, 1
	v_mul_lo_u32 v52, v51, s0
	s_cbranch_scc1 .LBB0_817
	v_add_u32_e32 v0, v52, v98
	v_lshl_add_u64 v[42:43], v[0:1], 1, v[108:109]
	v_lshl_add_u32 v0, v51, 6, v100
	v_lshl_add_u64 v[44:45], v[0:1], 1, v[110:111]
	global_load_dwordx4 v[70:73], v[42:43], off offset:512
	global_load_dwordx4 v[74:77], v[44:45], off
.LBB0_817:
	s_mov_b32 s0, 0x3e38aa3b
	v_mul_f32_e32 v20, s0, v20
	v_mul_f32_e32 v21, s0, v21
	v_mul_f32_e32 v18, s0, v18
	v_mul_f32_e32 v19, s0, v19
	v_mul_f32_e32 v16, s0, v16
	v_mul_f32_e32 v17, s0, v17
	s_mov_b64 vcc, s[4:5]
	v_cvt_pk_bf16_f32 v82, v20, v21
	v_mul_f32_e32 v20, s0, v26
	v_mul_f32_e32 v21, s0, v27
	v_cvt_pk_bf16_f32 v86, v18, v19
	v_mul_f32_e32 v18, s0, v24
	v_mul_f32_e32 v19, s0, v25
	v_cvt_pk_bf16_f32 v90, v16, v17
	v_mul_f32_e32 v16, s0, v22
	v_mul_f32_e32 v17, s0, v23
	v_mov_b32_e32 v5, v7
	v_cndmask_b32_sdwa v78, v1, v3, vcc dst_sel:DWORD dst_unused:UNUSED_PAD src0_sel:DWORD src1_sel:WORD_0
	v_cvt_pk_bf16_f32 v83, v20, v21
	v_mul_f32_e32 v20, s0, v32
	v_mul_f32_e32 v21, s0, v33
	v_cvt_pk_bf16_f32 v87, v18, v19
	v_mul_f32_e32 v18, s0, v30
	v_mul_f32_e32 v19, s0, v31
	v_cvt_pk_bf16_f32 v91, v16, v17
	v_mul_f32_e32 v16, s0, v28
	v_mul_f32_e32 v17, s0, v29
	v_mov_b32_e32 v11, v15
	v_mul_f32_e32 v4, s0, v4
	v_mul_f32_e32 v5, s0, v5
	v_mov_b32_e32 v7, v13
	v_mov_b32_e32 v3, v9
	v_cvt_pk_bf16_f32 v84, v20, v21
	v_mul_f32_e32 v20, s0, v38
	v_mul_f32_e32 v21, s0, v39
	v_cvt_pk_bf16_f32 v88, v18, v19
	v_mul_f32_e32 v18, s0, v36
	v_mul_f32_e32 v19, s0, v37
	v_cvt_pk_bf16_f32 v92, v16, v17
	v_mul_f32_e32 v16, s0, v34
	v_mul_f32_e32 v17, s0, v35
	v_mul_f32_e32 v10, s0, v10
	v_mul_f32_e32 v11, s0, v11
	v_cvt_pk_bf16_f32 v95, v4, v5
	v_mul_f32_e32 v4, s0, v6
	v_mul_f32_e32 v5, s0, v7
	v_mul_f32_e32 v2, s0, v2
	v_mul_f32_e32 v3, s0, v3
	v_cndmask_b32_e64 v0, 0, 1, s[28:29]
	v_mov_b32_e32 v79, v1
	v_mov_b32_e32 v80, v1
	v_mov_b32_e32 v81, v1
	v_cvt_pk_bf16_f32 v85, v20, v21
	v_cvt_pk_bf16_f32 v89, v18, v19
	v_cvt_pk_bf16_f32 v93, v16, v17
	v_cvt_pk_bf16_f32 v94, v10, v11
	v_cvt_pk_bf16_f32 v96, v4, v5
	v_cvt_pk_bf16_f32 v97, v2, v3
	v_cmp_ne_u32_e64 s[8:9], 1, v0
	s_andn2_b64 vcc, exec, s[28:29]
	v_mov_b32_e32 v18, 0
	s_cbranch_vccnz .LBB0_820
	v_sub_u32_e32 v0, v40, v114
	ds_read_b128 v[136:139], v115 offset:8192
	ds_read_b128 v[140:143], v115 offset:8224
	ds_read_b128 v[144:147], v115 offset:8256
	ds_read_b128 v[148:151], v115 offset:8288
	ds_read_b128 v[196:199], v115 offset:12800
	ds_read_b128 v[200:203], v115 offset:12832
	ds_read_b128 v[206:209], v115 offset:12864
	ds_read_b128 v[210:213], v115 offset:12896
	v_max_i32_e32 v184, -1, v0
	v_add_u32_e32 v184, 1, v184
	v_min_u32_e32 v184, 0x81, v184
	v_lshl_add_u32 v184, v184, 2, v122
	ds_read_b32 v184, v184 offset:2112
	v_add_u32_e32 v185, v40, v116
	v_max_i32_e32 v185, -1, v185
	v_add_u32_e32 v185, 1, v185
	v_min_u32_e32 v185, 0x81, v185
	v_lshl_add_u32 v185, v185, 2, v122
	ds_read_b32 v185, v185 offset:2112
	v_add_u32_e32 v186, -2, v0
	v_max_i32_e32 v186, -1, v186
	v_add_u32_e32 v186, 1, v186
	v_min_u32_e32 v186, 0x81, v186
	v_lshl_add_u32 v186, v186, 2, v122
	ds_read_b32 v186, v186 offset:2112
	v_add_u32_e32 v187, -3, v0
	v_max_i32_e32 v187, -1, v187
	v_add_u32_e32 v187, 1, v187
	v_min_u32_e32 v187, 0x81, v187
	v_lshl_add_u32 v187, v187, 2, v122
	ds_read_b32 v187, v187 offset:2112
	s_waitcnt lgkmcnt(11)
	v_mfma_f32_32x32x16_bf16 v[18:33], v[136:139], v[82:85], 0
	v_add_u32_e32 v188, -8, v0
	v_max_i32_e32 v188, -1, v188
	v_add_u32_e32 v188, 1, v188
	v_min_u32_e32 v188, 0x81, v188
	v_lshl_add_u32 v188, v188, 2, v122
	ds_read_b32 v188, v188 offset:2112
	s_waitcnt lgkmcnt(11)
	v_mfma_f32_32x32x16_bf16 v[18:33], v[140:143], v[86:89], v[18:33]
	v_add_u32_e32 v189, -9, v0
	v_max_i32_e32 v189, -1, v189
	v_add_u32_e32 v189, 1, v189
	v_min_u32_e32 v189, 0x81, v189
	v_lshl_add_u32 v189, v189, 2, v122
	ds_read_b32 v189, v189 offset:2112
	s_waitcnt lgkmcnt(11)
; #define LAS __attribute__((address_space(3)))
; __device__ __forceinline__ void swa_tile(const LAS unsigned char* Kb, const LAS unsigned char* Vb, const LAS float* btab, const bf16x8 (&Qf)[4], const bf16x8 qx, f32x16 (&O)[2],
;                                          float& lsum, int qpos, int k0, int l31, int hi) {
;     ...
;     for (int kb = 0; kb < 2; ++kb) {
;         f32x16 acc;
; #pragma unroll
;         for (int r = 0; r < 16; ++r) acc[r] = 0.f;
; #pragma unroll
;         for (int s = 0; s < 4; ++s) { const bf16x8 kf = *(const LAS bf16x8*)(Kb + (32 * kb + l31) * DF_PITCH + s * 32 + hi * 16);
;             acc = __builtin_amdgcn_mfma_f32_32x32x16_bf16(kf, Qf[s], acc, 0, 0, 0); }
;         acc = __builtin_amdgcn_mfma_f32_32x32x16_bf16(kx, qx, acc, 0, 0, 0);
;         S[kb] = acc;
;     }
;     float ls = 0.f;
;     bf16x8 Pf[4];
; #pragma unroll
;     for (int kb = 0; kb < 2; ++kb) {
; #pragma unroll
;         for (int r = 0; r < 16; ++r) { const int j = k0 + 32 * kb + (r & 3) + 8 * (r >> 2) + 4 * hi, dist = qpos - j;
;             const LAS float* tb = (k0 == 0 && kb == 0 && r < 8) ? btab + 4 * 132 : btab;
;             const float pv = __builtin_amdgcn_exp2f(S[kb][r] + tb[min(max(dist + 1, 0), 129)]); ls += pv; S[kb][r] = pv; }
	v_mfma_f32_32x32x16_bf16 v[18:33], v[144:147], v[90:93], v[18:33]
	v_add_u32_e32 v194, -10, v0
	v_max_i32_e32 v194, -1, v194
	v_add_u32_e32 v194, 1, v194
	v_min_u32_e32 v194, 0x81, v194
	v_lshl_add_u32 v194, v194, 2, v122
	ds_read_b32 v194, v194 offset:2112
	s_waitcnt lgkmcnt(11)
	v_mfma_f32_32x32x16_bf16 v[18:33], v[148:151], v[94:97], v[18:33]
	v_subrev_u32_e32 v195, 32, v0
	v_max_i32_e32 v195, -1, v195
	v_add_u32_e32 v195, 1, v195
	v_min_u32_e32 v195, 0x81, v195
	v_lshl_add_u32 v195, v195, 2, v122
	ds_read_b32 v195, v195
	s_waitcnt lgkmcnt(11)
	v_mfma_f32_32x32x16_bf16 v[2:17], v[196:199], v[82:85], 0
	v_add_u32_e32 v229, -11, v0
	v_max_i32_e32 v229, -1, v229
	v_add_u32_e32 v229, 1, v229
	v_min_u32_e32 v229, 0x81, v229
	v_lshl_add_u32 v229, v229, 2, v122
	ds_read_b32 v229, v229 offset:2112
	s_waitcnt lgkmcnt(11)
	v_mfma_f32_32x32x16_bf16 v[2:17], v[200:203], v[86:89], v[2:17]
	v_add_u32_e32 v230, -16, v0
	v_max_i32_e32 v230, -1, v230
	v_add_u32_e32 v230, 1, v230
	v_min_u32_e32 v230, 0x81, v230
	v_lshl_add_u32 v230, v230, 2, v122
	ds_read_b32 v230, v230
	s_waitcnt lgkmcnt(11)
	v_mfma_f32_32x32x16_bf16 v[2:17], v[206:209], v[90:93], v[2:17]
	v_subrev_u32_e32 v231, 33, v0
	v_max_i32_e32 v231, -1, v231
	v_add_u32_e32 v231, 1, v231
	v_min_u32_e32 v231, 0x81, v231
	v_lshl_add_u32 v231, v231, 2, v122
	ds_read_b32 v231, v231
	s_waitcnt lgkmcnt(11)
	v_mfma_f32_32x32x16_bf16 v[2:17], v[210:213], v[94:97], v[2:17]
	v_subrev_u32_e32 v248, 17, v0
	v_max_i32_e32 v248, -1, v248
	v_add_u32_e32 v248, 1, v248
	v_min_u32_e32 v248, 0x81, v248
	v_lshl_add_u32 v248, v248, 2, v122
	ds_read_b32 v248, v248
	v_mfma_f32_32x32x16_bf16 v[18:33], v[66:69], v[78:81], v[18:33]
	v_mfma_f32_32x32x16_bf16 v[2:17], v[66:69], v[78:81], v[2:17]
	s_nop 9
	s_waitcnt lgkmcnt(11)
	v_add_f32_e32 v18, v18, v184
	v_subrev_u32_e32 v184, 18, v0
	v_max_i32_e32 v184, -1, v184
	v_add_u32_e32 v184, 1, v184
	v_min_u32_e32 v184, 0x81, v184
	v_lshl_add_u32 v184, v184, 2, v122
	ds_read_b32 v184, v184
	v_exp_f32_e32 v18, v18
	s_waitcnt lgkmcnt(11)
	v_add_f32_e32 v19, v19, v185
	v_subrev_u32_e32 v185, 34, v0
	v_max_i32_e32 v185, -1, v185
	v_add_u32_e32 v185, 1, v185
	v_min_u32_e32 v185, 0x81, v185
	v_lshl_add_u32 v185, v185, 2, v122
	ds_read_b32 v185, v185
	v_exp_f32_e32 v19, v19
	s_waitcnt lgkmcnt(11)
	v_add_f32_e32 v20, v20, v186
	v_subrev_u32_e32 v186, 19, v0
	v_max_i32_e32 v186, -1, v186
	v_add_u32_e32 v186, 1, v186
	v_min_u32_e32 v186, 0x81, v186
	v_lshl_add_u32 v186, v186, 2, v122
	ds_read_b32 v186, v186
	v_cvt_pk_bf16_f32 v38, v18, v19
	v_add_f32_e32 v18, 0, v18
	v_add_f32_e32 v18, v18, v19
	s_waitcnt lgkmcnt(11)
	v_add_f32_e32 v21, v21, v187
	v_subrev_u32_e32 v187, 35, v0
	v_max_i32_e32 v187, -1, v187
	v_add_u32_e32 v187, 1, v187
	v_min_u32_e32 v187, 0x81, v187
	v_lshl_add_u32 v187, v187, 2, v122
	ds_read_b32 v187, v187
	s_waitcnt lgkmcnt(11)
	v_add_f32_e32 v22, v22, v188
	v_subrev_u32_e32 v188, 24, v0
	v_max_i32_e32 v188, -1, v188
	v_add_u32_e32 v188, 1, v188
	v_min_u32_e32 v188, 0x81, v188
	v_lshl_add_u32 v188, v188, 2, v122
	ds_read_b32 v188, v188
	v_exp_f32_e32 v20, v20
	v_exp_f32_e32 v21, v21
	v_exp_f32_e32 v22, v22
	s_waitcnt lgkmcnt(11)
	v_add_f32_e32 v23, v23, v189
	v_subrev_u32_e32 v189, 40, v0
	v_max_i32_e32 v189, -1, v189
	v_add_u32_e32 v189, 1, v189
	v_min_u32_e32 v189, 0x81, v189
	v_lshl_add_u32 v189, v189, 2, v122
	ds_read_b32 v189, v189
	v_exp_f32_e32 v23, v23
	v_add_f32_e32 v18, v18, v20
	v_add_f32_e32 v18, v18, v21
	v_add_f32_e32 v18, v18, v22
	s_waitcnt lgkmcnt(11)
	v_add_f32_e32 v24, v24, v194
	v_subrev_u32_e32 v194, 25, v0
	v_max_i32_e32 v194, -1, v194
	v_add_u32_e32 v194, 1, v194
	v_min_u32_e32 v194, 0x81, v194
	v_lshl_add_u32 v194, v194, 2, v122
	ds_read_b32 v194, v194
	s_waitcnt lgkmcnt(11)
	v_add_f32_e32 v2, v2, v195
	v_subrev_u32_e32 v195, 41, v0
	v_max_i32_e32 v195, -1, v195
	v_add_u32_e32 v195, 1, v195
	v_min_u32_e32 v195, 0x81, v195
	v_lshl_add_u32 v195, v195, 2, v122
	ds_read_b32 v195, v195
	s_waitcnt lgkmcnt(11)
	v_add_f32_e32 v25, v25, v229
	v_subrev_u32_e32 v229, 26, v0
	v_max_i32_e32 v229, -1, v229
	v_add_u32_e32 v229, 1, v229
	v_min_u32_e32 v229, 0x81, v229
	v_lshl_add_u32 v229, v229, 2, v122
	ds_read_b32 v229, v229
	v_exp_f32_e32 v24, v24
	s_waitcnt lgkmcnt(11)
	v_add_f32_e32 v26, v26, v230
	v_subrev_u32_e32 v230, 42, v0
	v_max_i32_e32 v230, -1, v230
	v_add_u32_e32 v230, 1, v230
	v_min_u32_e32 v230, 0x81, v230
	v_lshl_add_u32 v230, v230, 2, v122
	ds_read_b32 v230, v230
	s_waitcnt lgkmcnt(11)
	v_add_f32_e32 v3, v3, v231
	v_subrev_u32_e32 v231, 27, v0
	v_max_i32_e32 v231, -1, v231
	v_add_u32_e32 v231, 1, v231
	v_min_u32_e32 v231, 0x81, v231
	v_lshl_add_u32 v231, v231, 2, v122
	ds_read_b32 v231, v231
	s_waitcnt lgkmcnt(11)
	v_add_f32_e32 v27, v27, v248
	v_subrev_u32_e32 v248, 43, v0
	v_max_i32_e32 v248, -1, v248
	v_add_u32_e32 v248, 1, v248
	v_min_u32_e32 v248, 0x81, v248
	v_lshl_add_u32 v248, v248, 2, v122
	ds_read_b32 v248, v248
	v_exp_f32_e32 v25, v25
	v_exp_f32_e32 v26, v26
	v_exp_f32_e32 v27, v27
	s_waitcnt lgkmcnt(11)
	v_add_f32_e32 v28, v28, v184
	v_subrev_u32_e32 v184, 48, v0
	v_max_i32_e32 v184, -1, v184
	v_add_u32_e32 v184, 1, v184
	v_min_u32_e32 v184, 0x81, v184
	v_lshl_add_u32 v184, v184, 2, v122
	ds_read_b32 v184, v184
	s_waitcnt lgkmcnt(11)
; #define LAS __attribute__((address_space(3)))
; __device__ __forceinline__ void swa_tile(const LAS unsigned char* Kb, const LAS unsigned char* Vb, const LAS float* btab, const bf16x8 (&Qf)[4], const bf16x8 qx, f32x16 (&O)[2],
;                                          float& lsum, int qpos, int k0, int l31, int hi) {
;     ...
;     float ls = 0.f;
;     bf16x8 Pf[4];
; #pragma unroll
;     for (int kb = 0; kb < 2; ++kb) {
; #pragma unroll
;         for (int r = 0; r < 16; ++r) { const int j = k0 + 32 * kb + (r & 3) + 8 * (r >> 2) + 4 * hi, dist = qpos - j;
;             const LAS float* tb = (k0 == 0 && kb == 0 && r < 8) ? btab + 4 * 132 : btab;
;             const float pv = __builtin_amdgcn_exp2f(S[kb][r] + tb[min(max(dist + 1, 0), 129)]); ls += pv; S[kb][r] = pv; }
; #pragma unroll
;         for (int s = 0; s < 2; ++s) Pf[2 * kb + s] = pack_acc(S[kb], s);
;     }
;     lsum += ls;
; #pragma unroll
;     for (int st = 0; st < 4; ++st) { asm volatile("" ::: "memory");
; #pragma unroll
;         for (int dvb = 0; dvb < 2; ++dvb) { const bf16x8 vf = *(const LAS bf16x8*)(Vb + (32 * dvb + l31) * DF_PITCH + st * 32 + hi * 16);
;             O[dvb] = __builtin_amdgcn_mfma_f32_32x32x16_bf16(vf, Pf[st], O[dvb], 0, 0, 0); } }
	v_add_f32_e32 v4, v4, v185
	v_subrev_u32_e32 v185, 49, v0
	v_max_i32_e32 v185, -1, v185
	v_add_u32_e32 v185, 1, v185
	v_min_u32_e32 v185, 0x81, v185
	v_lshl_add_u32 v185, v185, 2, v122
	ds_read_b32 v185, v185
	v_add_f32_e32 v18, v18, v23
	v_exp_f32_e32 v28, v28
	v_add_f32_e32 v18, v18, v24
	s_waitcnt lgkmcnt(11)
	v_add_f32_e32 v29, v29, v186
	v_subrev_u32_e32 v186, 50, v0
	v_max_i32_e32 v186, -1, v186
	v_add_u32_e32 v186, 1, v186
	v_min_u32_e32 v186, 0x81, v186
	v_lshl_add_u32 v186, v186, 2, v122
	ds_read_b32 v186, v186
	s_waitcnt lgkmcnt(11)
	v_add_f32_e32 v5, v5, v187
	v_subrev_u32_e32 v187, 51, v0
	v_max_i32_e32 v187, -1, v187
	v_add_u32_e32 v187, 1, v187
	v_min_u32_e32 v187, 0x81, v187
	v_lshl_add_u32 v187, v187, 2, v122
	ds_read_b32 v187, v187
	v_exp_f32_e32 v29, v29
	v_add_f32_e32 v18, v18, v25
	v_add_f32_e32 v18, v18, v26
	s_waitcnt lgkmcnt(11)
	v_add_f32_e32 v30, v30, v188
	v_subrev_u32_e32 v188, 56, v0
	v_max_i32_e32 v188, -1, v188
	v_add_u32_e32 v188, 1, v188
	v_min_u32_e32 v188, 0x81, v188
	v_lshl_add_u32 v188, v188, 2, v122
	ds_read_b32 v188, v188
	s_waitcnt lgkmcnt(11)
	v_add_f32_e32 v6, v6, v189
	v_subrev_u32_e32 v189, 57, v0
	v_max_i32_e32 v189, -1, v189
	v_add_u32_e32 v189, 1, v189
	v_min_u32_e32 v189, 0x81, v189
	v_lshl_add_u32 v189, v189, 2, v122
	ds_read_b32 v189, v189
	v_exp_f32_e32 v30, v30
	v_add_f32_e32 v18, v18, v27
	v_add_f32_e32 v18, v18, v28
	s_waitcnt lgkmcnt(11)
	v_add_f32_e32 v31, v31, v194
	v_subrev_u32_e32 v194, 58, v0
	v_max_i32_e32 v194, -1, v194
	v_add_u32_e32 v194, 1, v194
	v_min_u32_e32 v194, 0x81, v194
	v_lshl_add_u32 v194, v194, 2, v122
	ds_read_b32 v194, v194
	s_waitcnt lgkmcnt(11)
	v_add_f32_e32 v7, v7, v195
	v_subrev_u32_e32 v195, 59, v0
	v_max_i32_e32 v195, -1, v195
	v_add_u32_e32 v195, 1, v195
	v_min_u32_e32 v195, 0x81, v195
	v_lshl_add_u32 v195, v195, 2, v122
	ds_read_b32 v195, v195
	v_exp_f32_e32 v31, v31
	v_add_f32_e32 v18, v18, v29
	v_add_f32_e32 v18, v18, v30
	s_waitcnt lgkmcnt(11)
	v_add_f32_e32 v32, v32, v229
	ds_read_b128 v[232:235], v115 offset:26624
	s_waitcnt lgkmcnt(11)
	v_add_f32_e32 v8, v8, v230
	ds_read_b128 v[236:239], v115 offset:31232
	v_exp_f32_e32 v32, v32
	v_exp_f32_e32 v2, v2
	v_exp_f32_e32 v3, v3
	s_waitcnt lgkmcnt(11)
	v_add_f32_e32 v33, v33, v231
	ds_read_b128 v[240:243], v115 offset:26656
	s_waitcnt lgkmcnt(11)
	v_add_f32_e32 v9, v9, v248
	ds_read_b128 v[244:247], v115 offset:31264
	v_exp_f32_e32 v33, v33
	v_add_f32_e32 v18, v18, v31
	v_add_f32_e32 v18, v18, v32
	v_exp_f32_e32 v4, v4
	s_waitcnt lgkmcnt(11)
	v_add_f32_e32 v10, v10, v184
	ds_read_b128 v[136:139], v115 offset:26688
	v_add_f32_e32 v18, v18, v33
	v_exp_f32_e32 v5, v5
	v_exp_f32_e32 v6, v6
	v_cvt_pk_bf16_f32 v46, v2, v3
	s_waitcnt lgkmcnt(11)
	v_add_f32_e32 v11, v11, v185
	ds_read_b128 v[140:143], v115 offset:31296
	v_add_f32_e32 v2, v18, v2
	v_exp_f32_e32 v7, v7
	v_add_f32_e32 v2, v2, v3
	v_exp_f32_e32 v8, v8
	s_waitcnt lgkmcnt(11)
	v_add_f32_e32 v12, v12, v186
	ds_read_b128 v[144:147], v115 offset:26720
	v_add_f32_e32 v2, v2, v4
	v_exp_f32_e32 v9, v9
	v_add_f32_e32 v2, v2, v5
	v_exp_f32_e32 v10, v10
	s_waitcnt lgkmcnt(11)
	v_add_f32_e32 v13, v13, v187
	ds_read_b128 v[148:151], v115 offset:31328
	v_add_f32_e32 v2, v2, v6
	v_exp_f32_e32 v11, v11
	v_add_f32_e32 v2, v2, v7
	v_exp_f32_e32 v12, v12
	s_waitcnt lgkmcnt(11)
	v_add_f32_e32 v14, v14, v188
	v_add_f32_e32 v2, v2, v8
	v_exp_f32_e32 v13, v13
	v_add_f32_e32 v2, v2, v9
	v_exp_f32_e32 v14, v14
	s_waitcnt lgkmcnt(10)
	v_add_f32_e32 v15, v15, v189
	v_add_f32_e32 v2, v2, v10
	v_exp_f32_e32 v15, v15
	s_waitcnt lgkmcnt(9)
	v_add_f32_e32 v16, v16, v194
	v_add_f32_e32 v2, v2, v11
	v_exp_f32_e32 v16, v16
	s_waitcnt lgkmcnt(8)
	v_add_f32_e32 v0, v17, v195
	v_add_f32_e32 v2, v2, v12
	v_exp_f32_e32 v0, v0
	v_add_f32_e32 v2, v2, v13
	v_add_f32_e32 v2, v2, v14
	v_add_f32_e32 v2, v2, v15
	v_add_f32_e32 v2, v2, v16
	v_cvt_pk_bf16_f32 v47, v4, v5
	v_cvt_pk_bf16_f32 v45, v16, v0
	v_add_f32_e32 v0, v2, v0
	v_cvt_pk_bf16_f32 v39, v20, v21
	v_cvt_pk_bf16_f32 v40, v22, v23
	v_cvt_pk_bf16_f32 v41, v24, v25
	v_cvt_pk_bf16_f32 v34, v26, v27
	v_cvt_pk_bf16_f32 v35, v28, v29
	v_cvt_pk_bf16_f32 v36, v30, v31
	v_cvt_pk_bf16_f32 v37, v32, v33
	s_waitcnt lgkmcnt(7)
	v_mfma_f32_32x32x16_bf16 v[18:33], v[232:235], v[38:41], 0
	v_cvt_pk_bf16_f32 v48, v6, v7
	v_cvt_pk_bf16_f32 v49, v8, v9
	v_cvt_pk_bf16_f32 v42, v10, v11
	v_cvt_pk_bf16_f32 v43, v12, v13
	v_cvt_pk_bf16_f32 v44, v14, v15
	s_waitcnt lgkmcnt(6)
	v_mfma_f32_32x32x16_bf16 v[2:17], v[236:239], v[38:41], 0
	v_add_f32_e32 v121, v121, v0
	s_waitcnt lgkmcnt(5)
	v_mfma_f32_32x32x16_bf16 v[18:33], v[240:243], v[34:37], v[18:33]
	s_waitcnt lgkmcnt(4)
	v_mfma_f32_32x32x16_bf16 v[2:17], v[244:247], v[34:37], v[2:17]
	s_waitcnt lgkmcnt(3)
	v_mfma_f32_32x32x16_bf16 v[18:33], v[136:139], v[46:49], v[18:33]
	s_waitcnt lgkmcnt(2)
	v_mfma_f32_32x32x16_bf16 v[2:17], v[140:143], v[46:49], v[2:17]
	s_waitcnt lgkmcnt(1)
	v_mfma_f32_32x32x16_bf16 v[18:33], v[144:147], v[42:45], v[18:33]
	s_waitcnt lgkmcnt(0)
	v_mfma_f32_32x32x16_bf16 v[2:17], v[148:151], v[42:45], v[2:17]
	v_cndmask_b32_e64 v0, 0, 1, s[30:31]
	v_cmp_ne_u32_e64 s[0:1], 1, v0
	s_andn2_b64 vcc, exec, s[30:31]
	s_cbranch_vccz .LBB0_821
	s_branch .LBB0_822

; __device__ __forceinline__ int lt_tid(int wv) { int ln; asm volatile("v_mbcnt_lo_u32_b32 %0, -1, 0\n\tv_mbcnt_hi_u32_b32 %0, -1, %0" : "=v"(ln)); return (wv << 6) | ln; }
; __device__ __forceinline__ unsigned pkbf(float lo, float hi) { f32x2_t v = {lo, hi}; bf16x2_t b = __builtin_convertvector(v, bf16x2_t); return __builtin_bit_cast(unsigned, b); }
;     ...
;         const float lt = lsum + __shfl_xor(lsum, 32), inv = 1.0f / lt;
;         const int lane2 = lt_tid(wvid) & 63, qpos2 = q0w + (lane2 & 31), hi2 = lane2 >> 5;
;         if (wave_on && qpos2 < LT && (qi > 0 || qpos2 < NMETA)) {
;             bf16_t* orow = MIX + ((size_t)b * LT + qpos2) * D + M_A + hq * 64;
; #pragma unroll
;             for (int d = 0; d < 2; ++d)
; #pragma unroll
;                 for (int g4 = 0; g4 < 4; ++g4) { const int dv0 = 32 * d + 8 * g4 + 4 * hi2;
;                     u32x2 w; w.x = pkbf(O[d][4 * g4] * inv, O[d][4 * g4 + 1] * inv); w.y = pkbf(O[d][4 * g4 + 2] * inv, O[d][4 * g4 + 3] * inv);
;                     *(u32x2*)(orow + dv0) = w; }
.LBB0_833:
	ds_bpermute_b32 v35, v103, v121
	v_mbcnt_lo_u32_b32 v34, -1, 0
	v_mbcnt_hi_u32_b32 v34, -1, v34
	s_and_b64 s[0:1], s[6:7], exec
	v_and_b32_e32 v0, 31, v34
	v_add_u32_e32 v0, v0, v120
	s_cselect_b32 s0, 0x1010, 16
	v_cmp_gt_i32_e32 vcc, s0, v0
	s_and_b64 s[0:1], s[28:29], vcc
	s_and_saveexec_b64 s[6:7], s[0:1]
	s_xor_b64 s[0:1], exec, s[6:7]
	s_cbranch_execz .LBB0_805
	s_waitcnt lgkmcnt(0)
	v_add_f32_e32 v35, v121, v35
	v_div_scale_f32 v36, s[6:7], v35, v35, 1.0
	v_rcp_f32_e32 v37, v36
	v_div_scale_f32 v38, vcc, 1.0, v35, 1.0
	v_fma_f32 v39, -v36, v37, 1.0
	v_fmac_f32_e32 v37, v39, v37
	v_mul_f32_e32 v39, v38, v37
	v_fma_f32 v40, -v36, v39, v38
	v_fmac_f32_e32 v39, v40, v37
	v_fma_f32 v36, -v36, v39, v38
	v_div_fmas_f32 v36, v36, v37, v39
	v_lshl_add_u64 v[38:39], v[0:1], 0, v[104:105]
	v_lshlrev_b64 v[38:39], 11, v[38:39]
	v_div_fixup_f32 v36, v36, v35, 1.0
	v_lshl_add_u64 v[38:39], s[20:21], 0, v[38:39]
	v_lshrrev_b32_e32 v0, 2, v34
	v_lshl_add_u64 v[38:39], v[106:107], 1, v[38:39]
	v_mul_f32_e32 v18, v18, v36
	v_mul_f32_e32 v19, v19, v36
	v_mul_f32_e32 v20, v20, v36
	v_mul_f32_e32 v21, v21, v36
	v_and_b32_e32 v0, 8, v0
	v_mul_f32_e32 v2, v2, v36
	v_mul_f32_e32 v3, v3, v36
	v_mul_f32_e32 v4, v4, v36
	v_mul_f32_e32 v5, v5, v36
	v_cvt_pk_bf16_f32 v18, v18, v19
	v_cvt_pk_bf16_f32 v19, v20, v21
	v_lshl_add_u64 v[20:21], v[38:39], 0, v[0:1]
	v_cvt_pk_bf16_f32 v2, v2, v3
	v_cvt_pk_bf16_f32 v3, v4, v5
	global_store_dwordx2 v[20:21], v[18:19], off
	v_mul_f32_e32 v18, v22, v36
	v_mul_f32_e32 v19, v23, v36
	v_mul_f32_e32 v22, v24, v36
	v_mul_f32_e32 v23, v25, v36
	global_store_dwordx2 v[20:21], v[2:3], off offset:64
	v_mul_f32_e32 v2, v6, v36
	v_mul_f32_e32 v3, v7, v36
	v_mul_f32_e32 v4, v8, v36
	v_mul_f32_e32 v5, v9, v36
	v_cvt_pk_bf16_f32 v18, v18, v19
	v_cvt_pk_bf16_f32 v19, v22, v23
	v_cvt_pk_bf16_f32 v2, v2, v3
	v_cvt_pk_bf16_f32 v3, v4, v5
	global_store_dwordx2 v[20:21], v[18:19], off offset:16
	v_mul_f32_e32 v18, v26, v36
	v_mul_f32_e32 v19, v27, v36
	v_mul_f32_e32 v22, v28, v36
	v_mul_f32_e32 v23, v29, v36
	global_store_dwordx2 v[20:21], v[2:3], off offset:80
	v_mul_f32_e32 v2, v10, v36
	v_mul_f32_e32 v3, v11, v36
	v_mul_f32_e32 v4, v12, v36
	v_mul_f32_e32 v5, v13, v36
	v_cvt_pk_bf16_f32 v18, v18, v19
	v_cvt_pk_bf16_f32 v19, v22, v23
	v_cvt_pk_bf16_f32 v2, v2, v3
	v_cvt_pk_bf16_f32 v3, v4, v5
	global_store_dwordx2 v[20:21], v[18:19], off offset:32
	v_mul_f32_e32 v18, v30, v36
	v_mul_f32_e32 v19, v31, v36
	v_mul_f32_e32 v22, v32, v36
	v_mul_f32_e32 v23, v33, v36
	global_store_dwordx2 v[20:21], v[2:3], off offset:96
	v_mul_f32_e32 v2, v14, v36
	v_mul_f32_e32 v3, v15, v36
	v_mul_f32_e32 v4, v16, v36
	v_mul_f32_e32 v5, v17, v36
	v_cvt_pk_bf16_f32 v18, v18, v19
	v_cvt_pk_bf16_f32 v19, v22, v23
	v_cvt_pk_bf16_f32 v2, v2, v3
	v_cvt_pk_bf16_f32 v3, v4, v5
	global_store_dwordx2 v[20:21], v[18:19], off offset:48
	global_store_dwordx2 v[20:21], v[2:3], off offset:112
	s_branch .LBB0_805
